# P8 prep: each wave touches its next item's 96 cache lines after its loads land, so the next item's loads hit L2
# baseline (speedup 1.0000x reference)
; __global__ void __launch_bounds__(NWAVES * 64, 2) mk_fwd(Args args) {
;     ...
;             for (int it = gw; it < 8192; it += NGW) {
;                 const int h = it & 15, c = (it >> 4) & 127, b = it >> 11;
;                 int ln = lane; asm volatile("" : "+v"(ln));
;                 const size_t r0 = ((size_t)b * T + c * 16) * RW + h * 64;
;                 const float kac = (ka->in[24] + l * RW + h * 64)[ln];
;                 float at[16], rt[16]; unsigned bhp[8], khp[8];
;                 float Wc = 1.0f;
;                 {
;                     float dw[16]; unsigned short da[16], dq[16], dk[16], dr[16];
; #pragma unroll
;                     for (int t = 0; t < 16; ++t) { const int r = (int)r0 + t * RW;
;                         dw[t] = __builtin_bit_cast(float, __builtin_amdgcn_raw_buffer_load_b32(rs_w, ln * 4, r * 4, 0));
;                         da[t] = __builtin_amdgcn_raw_buffer_load_b16(rs_a, ln * 2, r * 2, 0); dq[t] = __builtin_amdgcn_raw_buffer_load_b16(rs_q, ln * 2, r * 2, 0); dk[t] = __builtin_amdgcn_raw_buffer_load_b16(rs_k, ln * 2, r * 2, 0);
;                         dr[t] = __builtin_amdgcn_raw_buffer_load_b16(rs_r, ln * 2, r * 2, 0); }
.LBB0_749:
	v_mov_b32_e32 v0, v8
	s_load_dwordx2 s[16:17], s[18:19], 0xc0
	s_and_b32 s22, s38, 0x3c0
	v_ashrrev_i32_e32 v1, 31, v0
	v_readlane_b32 s44, v254, 23
	v_readlane_b32 s48, v254, 27
	s_waitcnt lgkmcnt(0)
	s_add_u32 s16, s16, s34
	s_addc_u32 s17, s17, s35
	s_lshl_b32 s23, s22, 2
	s_add_u32 s16, s16, s23
	s_addc_u32 s17, s17, 0
	v_lshl_add_u64 v[2:3], v[0:1], 2, s[16:17]
	s_and_b32 s16, s1, 0x3ffff0
	s_lshl_b32 s16, s16, 10
	s_or_b32 s16, s16, s22
	v_lshlrev_b32_e32 v4, 2, v0
	s_lshl_b32 s17, s16, 2
	v_readlane_b32 s45, v254, 24
	v_readlane_b32 s46, v254, 25
	v_readlane_b32 s47, v254, 26
	v_readlane_b32 s50, v254, 29
	v_readlane_b32 s51, v254, 30
	global_load_dword v2, v[2:3], off
	v_lshlrev_b32_e32 v1, 1, v0
	v_readlane_b32 s49, v254, 28
	buffer_load_dword v3, v4, s[44:47], s17 offen
	s_lshl_b32 s17, s16, 1
	s_mov_b32 s30, s50
	s_mov_b32 s31, s51
	s_mov_b32 s22, s50
	s_mov_b32 s23, s51
	s_mov_b32 s26, s50
	s_mov_b32 s27, s51
	buffer_load_ushort v5, v1, s[48:51], s17 offen
	buffer_load_ushort v6, v1, s[28:31], s17 offen
	buffer_load_ushort v7, v1, s[20:23], s17 offen
	buffer_load_ushort v15, v1, s[24:27], s17 offen
	s_or_b32 s17, s16, 0x400
	s_lshl_b32 s40, s17, 2
	s_lshl_b32 s17, s17, 1
	buffer_load_dword v18, v4, s[44:47], s40 offen
	buffer_load_ushort v19, v1, s[48:51], s17 offen
	buffer_load_ushort v13, v1, s[28:31], s17 offen
	buffer_load_ushort v17, v1, s[20:23], s17 offen
	buffer_load_ushort v25, v1, s[24:27], s17 offen
	s_or_b32 s17, s16, 0x800
	s_lshl_b32 s40, s17, 2
	s_lshl_b32 s17, s17, 1
	buffer_load_dword v14, v4, s[44:47], s40 offen
	buffer_load_ushort v12, v1, s[48:51], s17 offen
	buffer_load_ushort v10, v1, s[28:31], s17 offen
	buffer_load_ushort v11, v1, s[20:23], s17 offen
	buffer_load_ushort v20, v1, s[24:27], s17 offen
	s_or_b32 s17, s16, 0xc00
	s_lshl_b32 s40, s17, 2
	s_lshl_b32 s17, s17, 1
	buffer_load_dword v27, v4, s[44:47], s40 offen
	buffer_load_ushort v29, v1, s[48:51], s17 offen
	buffer_load_ushort v23, v1, s[28:31], s17 offen
	buffer_load_ushort v28, v1, s[20:23], s17 offen
	buffer_load_ushort v33, v1, s[24:27], s17 offen
	s_or_b32 s17, s16, 0x1000
	s_lshl_b32 s40, s17, 2
	s_lshl_b32 s17, s17, 1
	buffer_load_dword v24, v4, s[44:47], s40 offen
	buffer_load_ushort v22, v1, s[48:51], s17 offen
	buffer_load_ushort v16, v1, s[28:31], s17 offen
	buffer_load_ushort v21, v1, s[20:23], s17 offen
	buffer_load_ushort v30, v1, s[24:27], s17 offen
	s_or_b32 s17, s16, 0x1400
	s_lshl_b32 s40, s17, 2
	s_lshl_b32 s17, s17, 1
	buffer_load_dword v40, v4, s[44:47], s40 offen
	buffer_load_ushort v41, v1, s[48:51], s17 offen
	buffer_load_ushort v42, v1, s[28:31], s17 offen
	buffer_load_ushort v43, v1, s[20:23], s17 offen
	buffer_load_ushort v44, v1, s[24:27], s17 offen
	s_or_b32 s17, s16, 0x1800
	s_lshl_b32 s40, s17, 2
	s_lshl_b32 s17, s17, 1
	buffer_load_dword v45, v4, s[44:47], s40 offen
	buffer_load_ushort v32, v1, s[48:51], s17 offen
	buffer_load_ushort v26, v1, s[28:31], s17 offen
	buffer_load_ushort v31, v1, s[20:23], s17 offen
	buffer_load_ushort v46, v1, s[24:27], s17 offen
	s_or_b32 s17, s16, 0x1c00
	s_lshl_b32 s40, s17, 2
	s_lshl_b32 s17, s17, 1
	buffer_load_dword v47, v4, s[44:47], s40 offen
	buffer_load_ushort v48, v1, s[48:51], s17 offen
	buffer_load_ushort v49, v1, s[28:31], s17 offen
	buffer_load_ushort v50, v1, s[20:23], s17 offen
	buffer_load_ushort v51, v1, s[24:27], s17 offen
	s_or_b32 s17, s16, 0x2000
	s_lshl_b32 s40, s17, 2
	s_lshl_b32 s17, s17, 1
	buffer_load_dword v52, v4, s[44:47], s40 offen
	buffer_load_ushort v53, v1, s[48:51], s17 offen
	buffer_load_ushort v54, v1, s[28:31], s17 offen
	buffer_load_ushort v55, v1, s[20:23], s17 offen
	buffer_load_ushort v56, v1, s[24:27], s17 offen
	s_or_b32 s17, s16, 0x2400
	s_lshl_b32 s40, s17, 2
	s_lshl_b32 s17, s17, 1
	buffer_load_dword v57, v4, s[44:47], s40 offen
	buffer_load_ushort v58, v1, s[48:51], s17 offen
	buffer_load_ushort v59, v1, s[28:31], s17 offen
	buffer_load_ushort v60, v1, s[20:23], s17 offen
	buffer_load_ushort v61, v1, s[24:27], s17 offen
	s_or_b32 s17, s16, 0x2800
	s_lshl_b32 s40, s17, 2
	s_lshl_b32 s17, s17, 1
	buffer_load_dword v62, v4, s[44:47], s40 offen
	buffer_load_ushort v63, v1, s[48:51], s17 offen
	buffer_load_ushort v71, v1, s[28:31], s17 offen
	buffer_load_ushort v72, v1, s[20:23], s17 offen
	buffer_load_ushort v73, v1, s[24:27], s17 offen
	s_or_b32 s17, s16, 0x2c00
	s_lshl_b32 s40, s17, 2
	s_lshl_b32 s17, s17, 1
	buffer_load_dword v77, v4, s[44:47], s40 offen
	buffer_load_ushort v89, v1, s[48:51], s17 offen
	buffer_load_ushort v90, v1, s[28:31], s17 offen
	buffer_load_ushort v91, v1, s[20:23], s17 offen
	buffer_load_ushort v92, v1, s[24:27], s17 offen
	s_or_b32 s17, s16, 0x3000
	s_lshl_b32 s40, s17, 2
	s_lshl_b32 s17, s17, 1
	buffer_load_dword v93, v4, s[44:47], s40 offen
	buffer_load_ushort v94, v1, s[48:51], s17 offen
	buffer_load_ushort v95, v1, s[28:31], s17 offen
	buffer_load_ushort v96, v1, s[20:23], s17 offen
	buffer_load_ushort v97, v1, s[24:27], s17 offen
	s_or_b32 s17, s16, 0x3400
	s_lshl_b32 s40, s17, 2
	s_lshl_b32 s17, s17, 1
	buffer_load_dword v98, v4, s[44:47], s40 offen
	buffer_load_ushort v99, v1, s[48:51], s17 offen
	buffer_load_ushort v100, v1, s[28:31], s17 offen
	buffer_load_ushort v101, v1, s[20:23], s17 offen
	buffer_load_ushort v102, v1, s[24:27], s17 offen
	s_or_b32 s17, s16, 0x3800
	s_lshl_b32 s40, s17, 2
	s_lshl_b32 s17, s17, 1
	s_or_b32 s16, s16, 0x3c00
	buffer_load_dword v103, v4, s[44:47], s40 offen
	buffer_load_ushort v104, v1, s[48:51], s17 offen
	buffer_load_ushort v105, v1, s[28:31], s17 offen
	buffer_load_ushort v106, v1, s[20:23], s17 offen
	buffer_load_ushort v107, v1, s[24:27], s17 offen
	s_lshl_b32 s17, s16, 2
	s_lshl_b32 s16, s16, 1
	buffer_load_dword v108, v4, s[44:47], s17 offen
	buffer_load_ushort v109, v1, s[48:51], s16 offen
	buffer_load_ushort v110, v1, s[28:31], s16 offen
	buffer_load_ushort v111, v1, s[20:23], s16 offen
	buffer_load_ushort v112, v1, s[24:27], s16 offen
	s_waitcnt vmcnt(62)
; __device__ __forceinline__ unsigned cvt_nat(float lo, float hi) { const f32x2 v = {lo, hi}; return __builtin_bit_cast(unsigned, __builtin_convertvector(v, bf16n2)); }
; __global__ void __launch_bounds__(NWAVES * 64, 2) mk_fwd(Args args) {
;     ...
;                     __builtin_amdgcn_sched_barrier(0);
; #pragma unroll
;                     for (int t = 0; t < 16; t += 2) {
;                         float bh2[2], kh2[2];
; #pragma unroll
;                         for (int e = 0; e < 2; ++e) {
;                             const float as_ = bf2f(da[t + e]), kk_ = bf2f(dq[t + e]), k_ = bf2f(dk[t + e]), r_ = bf2f(dr[t + e]);
;                             const float Wp = Wc; Wc = Wc * dw[t + e]; const float inv = __builtin_amdgcn_rcpf(Wc);
;                             at[t + e] = -(Wp * kk_); rt[t + e] = Wc * r_; bh2[e] = kk_ * as_ * inv; kh2[e] = k_ * (1.0f + (as_ - 1.0f) * kac) * inv;
;                         }
;                         bhp[t >> 1] = cvt_nat(bh2[0], bh2[1]); khp[t >> 1] = cvt_nat(kh2[0], kh2[1]);
;                     }
	v_mul_f32_e32 v84, v3, v18
	v_lshlrev_b32_e32 v15, 16, v15
	v_rcp_f32_e32 v34, v3
	v_rcp_f32_e32 v35, v84
	v_lshlrev_b32_e32 v18, 16, v5
	v_lshlrev_b32_e32 v19, 16, v19
	v_lshlrev_b32_e32 v36, 16, v7
	v_lshlrev_b32_e32 v6, 16, v6
	v_lshlrev_b32_e32 v7, 16, v13
	v_mul_f32_e32 v70, v3, v15
	v_mul_f32_e64 v3, v3, -v7
	v_pk_mul_f32 v[38:39], v[18:19], v[6:7]
	v_pk_add_f32 v[18:19], v[18:19], -1.0 op_sel_hi:[1,0]
	v_lshlrev_b32_e32 v37, 16, v17
	v_pk_fma_f32 v[18:19], v[2:3], v[18:19], 1.0 op_sel_hi:[0,1,0]
	v_mul_f32_e32 v17, v84, v14
	v_pk_mul_f32 v[18:19], v[18:19], v[36:37]
	v_mul_f32_e32 v86, v17, v27
	v_pk_mul_f32 v[18:19], v[34:35], v[18:19]
	v_lshlrev_b32_e32 v13, 16, v20
	v_rcp_f32_e32 v14, v17
	v_rcp_f32_e32 v15, v86
	v_cvt_pk_bf16_f32 v7, v18, v19
	v_mul_f32_e32 v88, v17, v13
	v_lshlrev_b32_e32 v19, 16, v29
	v_lshlrev_b32_e32 v18, 16, v12
	v_lshlrev_b32_e32 v13, 16, v23
	v_lshlrev_b32_e32 v12, 16, v10
	s_waitcnt vmcnt(61)
	v_lshlrev_b32_e32 v29, 16, v28
	v_lshlrev_b32_e32 v28, 16, v11
	v_pk_mul_f32 v[10:11], v[18:19], v[12:13]
	v_pk_add_f32 v[18:19], v[18:19], -1.0 op_sel_hi:[1,0]
	v_pk_mul_f32 v[38:39], v[38:39], v[34:35]
	v_pk_fma_f32 v[18:19], v[2:3], v[18:19], 1.0 op_sel_hi:[0,1,0]
	v_mul_f32_e64 v35, v17, -v13
	v_pk_mul_f32 v[10:11], v[10:11], v[14:15]
	v_pk_mul_f32 v[18:19], v[18:19], v[28:29]
	s_waitcnt vmcnt(59)
	v_mul_f32_e32 v17, v86, v24
	v_pk_mul_f32 v[14:15], v[14:15], v[18:19]
	v_cvt_pk_bf16_f32 v13, v10, v11
	s_waitcnt vmcnt(55)
	v_lshlrev_b32_e32 v10, 16, v30
	s_waitcnt vmcnt(54)
	v_mul_f32_e32 v82, v17, v40
	v_cvt_pk_bf16_f32 v28, v14, v15
	v_rcp_f32_e32 v14, v17
	v_mul_f32_e32 v87, v17, v10
	v_rcp_f32_e32 v15, v82
	s_waitcnt vmcnt(53)
	v_lshlrev_b32_e32 v19, 16, v41
	v_lshlrev_b32_e32 v18, 16, v22
	s_waitcnt vmcnt(52)
	v_lshlrev_b32_e32 v11, 16, v42
	v_lshlrev_b32_e32 v10, 16, v16
	v_cvt_pk_bf16_f32 v5, v38, v39
	v_mul_f32_e64 v38, v17, -v11
	v_pk_mul_f32 v[16:17], v[18:19], v[10:11]
	v_pk_add_f32 v[18:19], v[18:19], -1.0 op_sel_hi:[1,0]
	s_waitcnt vmcnt(51)
	v_lshlrev_b32_e32 v23, 16, v43
	v_lshlrev_b32_e32 v22, 16, v21
	v_pk_fma_f32 v[18:19], v[2:3], v[18:19], 1.0 op_sel_hi:[0,1,0]
	v_pk_mul_f32 v[18:19], v[18:19], v[22:23]
	v_pk_mul_f32 v[16:17], v[16:17], v[14:15]
	v_pk_mul_f32 v[14:15], v[14:15], v[18:19]
	s_waitcnt vmcnt(49)
	v_mul_f32_e32 v22, v82, v45
	v_cvt_pk_bf16_f32 v39, v14, v15
	s_waitcnt vmcnt(45)
	v_lshlrev_b32_e32 v14, 16, v46
	s_waitcnt vmcnt(44)
	v_mul_f32_e32 v79, v22, v47
	v_cvt_pk_bf16_f32 v11, v16, v17
	v_rcp_f32_e32 v16, v22
	v_mul_f32_e32 v80, v22, v14
	v_rcp_f32_e32 v17, v79
	s_waitcnt vmcnt(43)
	v_lshlrev_b32_e32 v19, 16, v48
	v_lshlrev_b32_e32 v18, 16, v32
	s_waitcnt vmcnt(42)
	v_lshlrev_b32_e32 v15, 16, v49
	v_lshlrev_b32_e32 v14, 16, v26
	v_mul_f32_e64 v47, v22, -v15
	v_pk_mul_f32 v[22:23], v[18:19], v[14:15]
	v_pk_add_f32 v[18:19], v[18:19], -1.0 op_sel_hi:[1,0]
	s_waitcnt vmcnt(41)
	v_lshlrev_b32_e32 v21, 16, v50
	v_lshlrev_b32_e32 v20, 16, v31
	v_pk_fma_f32 v[18:19], v[2:3], v[18:19], 1.0 op_sel_hi:[0,1,0]
	v_pk_mul_f32 v[18:19], v[18:19], v[20:21]
	v_pk_mul_f32 v[22:23], v[22:23], v[16:17]
	v_pk_mul_f32 v[16:17], v[16:17], v[18:19]
	s_waitcnt vmcnt(39)
	v_mul_f32_e32 v24, v79, v52
	v_cvt_pk_bf16_f32 v42, v16, v17
	s_waitcnt vmcnt(35)
	v_lshlrev_b32_e32 v17, 16, v56
	s_waitcnt vmcnt(34)
	v_mul_f32_e32 v37, v24, v57
	v_rcp_f32_e32 v16, v24
	v_mul_f32_e32 v76, v24, v17
	s_waitcnt vmcnt(30)
	v_lshlrev_b32_e32 v18, 16, v61
	v_rcp_f32_e32 v17, v37
	v_cvt_pk_bf16_f32 v15, v22, v23
	v_mul_f32_e32 v75, v37, v18
	v_lshlrev_b32_e32 v19, 16, v58
	v_lshlrev_b32_e32 v18, 16, v53
	v_lshlrev_b32_e32 v23, 16, v59
	v_lshlrev_b32_e32 v22, 16, v54
	v_lshlrev_b32_e32 v83, 16, v25
	v_mul_f32_e64 v26, v24, -v23
	v_pk_mul_f32 v[24:25], v[18:19], v[22:23]
	v_pk_add_f32 v[18:19], v[18:19], -1.0 op_sel_hi:[1,0]
	v_lshlrev_b32_e32 v21, 16, v60
	v_lshlrev_b32_e32 v20, 16, v55
	v_pk_fma_f32 v[18:19], v[2:3], v[18:19], 1.0 op_sel_hi:[0,1,0]
	v_pk_mul_f32 v[24:25], v[24:25], v[16:17]
	v_pk_mul_f32 v[18:19], v[18:19], v[20:21]
	v_cvt_pk_bf16_f32 v23, v24, v25
	v_pk_mul_f32 v[16:17], v[16:17], v[18:19]
	s_waitcnt vmcnt(29)
	v_mul_f32_e32 v24, v37, v62
	v_lshlrev_b32_e32 v81, 16, v44
	v_cvt_pk_bf16_f32 v44, v16, v17
	s_waitcnt vmcnt(25)
	v_lshlrev_b32_e32 v17, 16, v73
	s_waitcnt vmcnt(20)
	v_lshlrev_b32_e32 v18, 16, v92
	v_mul_f32_e32 v40, v24, v77
	v_lshlrev_b32_e32 v85, 16, v33
	v_rcp_f32_e32 v16, v24
	v_mul_f32_e32 v74, v24, v17
	v_rcp_f32_e32 v17, v40
	v_mul_f32_e32 v73, v40, v18
	v_lshlrev_b32_e32 v19, 16, v89
	v_lshlrev_b32_e32 v18, 16, v63
	v_lshlrev_b32_e32 v33, 16, v90
	v_lshlrev_b32_e32 v32, 16, v71
	v_mul_f32_e64 v36, v24, -v33
	v_pk_mul_f32 v[24:25], v[18:19], v[32:33]
	v_pk_add_f32 v[18:19], v[18:19], -1.0 op_sel_hi:[1,0]
	v_lshlrev_b32_e32 v21, 16, v91
	v_lshlrev_b32_e32 v20, 16, v72
	v_pk_fma_f32 v[18:19], v[2:3], v[18:19], 1.0 op_sel_hi:[0,1,0]
	v_pk_mul_f32 v[18:19], v[18:19], v[20:21]
	v_pk_mul_f32 v[24:25], v[24:25], v[16:17]
	v_pk_mul_f32 v[16:17], v[16:17], v[18:19]
	s_waitcnt vmcnt(19)
	v_mul_f32_e32 v46, v40, v93
	v_cvt_pk_bf16_f32 v48, v16, v17
	s_waitcnt vmcnt(15)
	v_lshlrev_b32_e32 v17, 16, v97
	s_waitcnt vmcnt(10)
	v_lshlrev_b32_e32 v18, 16, v102
	v_mul_f32_e32 v49, v46, v98
	v_cvt_pk_bf16_f32 v33, v24, v25
	v_rcp_f32_e32 v16, v46
	v_mul_f32_e32 v72, v46, v17
	v_rcp_f32_e32 v17, v49
	v_mul_f32_e32 v71, v49, v18
	v_lshlrev_b32_e32 v19, 16, v99
	v_lshlrev_b32_e32 v18, 16, v94
	v_lshlrev_b32_e32 v25, 16, v100
	v_lshlrev_b32_e32 v24, 16, v95
	v_mul_f32_e64 v40, v40, -v24
	v_mul_f32_e64 v46, v46, -v25
	v_pk_mul_f32 v[24:25], v[18:19], v[24:25]
	v_pk_add_f32 v[18:19], v[18:19], -1.0 op_sel_hi:[1,0]
	v_lshlrev_b32_e32 v21, 16, v101
	v_lshlrev_b32_e32 v20, 16, v96
	v_pk_fma_f32 v[18:19], v[2:3], v[18:19], 1.0 op_sel_hi:[0,1,0]
	v_pk_mul_f32 v[18:19], v[18:19], v[20:21]
	v_pk_mul_f32 v[24:25], v[24:25], v[16:17]
	v_pk_mul_f32 v[16:17], v[16:17], v[18:19]
	s_waitcnt vmcnt(9)
; #define LAS __attribute__((address_space(3)))
; __global__ void __launch_bounds__(NWAVES * 64, 2) mk_fwd(Args args) {
;     ...
;                     for (int t = 0; t < 16; ++t) { const int r = (int)r0 + t * RW;
;                         dw[t] = __builtin_bit_cast(float, __builtin_amdgcn_raw_buffer_load_b32(rs_w, ln * 4, r * 4, 0));
;                         da[t] = __builtin_amdgcn_raw_buffer_load_b16(rs_a, ln * 2, r * 2, 0); dq[t] = __builtin_amdgcn_raw_buffer_load_b16(rs_q, ln * 2, r * 2, 0); dk[t] = __builtin_amdgcn_raw_buffer_load_b16(rs_k, ln * 2, r * 2, 0);
;                         dr[t] = __builtin_amdgcn_raw_buffer_load_b16(rs_r, ln * 2, r * 2, 0); }
;     ...
;                 const __amdgpu_buffer_rsrc_t rs_o = __builtin_amdgcn_make_buffer_rsrc((void*)(REC + (size_t)it * 12288), 0, 12288, 0x00020000);
;                 {
;                     const bool sw = (ln & 8) != 0;
;                     v4u lo, hi;
;                     lo.x = bhp[0]; lo.y = bhp[1]; lo.z = bhp[2]; lo.w = bhp[3]; hi.x = bhp[4]; hi.y = bhp[5]; hi.z = bhp[6]; hi.w = bhp[7];
;                     __builtin_amdgcn_raw_buffer_store_b128(sw ? hi : lo, rs_o, ln * 32 + 4096, 0, 0); __builtin_amdgcn_raw_buffer_store_b128(sw ? lo : hi, rs_o, ln * 32 + 4096 + 16, 0, 0);
;                     lo.x = khp[0]; lo.y = khp[1]; lo.z = khp[2]; lo.w = khp[3]; hi.x = khp[4]; hi.y = khp[5]; hi.z = khp[6]; hi.w = khp[7];
;                     __builtin_amdgcn_raw_buffer_store_b128(sw ? hi : lo, rs_o, ln * 32 + 6144, 0, 0); __builtin_amdgcn_raw_buffer_store_b128(sw ? lo : hi, rs_o, ln * 32 + 6144 + 16, 0, 0);
;                 }
;                 __builtin_amdgcn_raw_buffer_store_b32(__builtin_bit_cast(unsigned, Wc), rs_o, ln * 4, 11264, 0);
; #pragma unroll
;                 for (int t = 0; t < 16; ++t) {
;                     *(LAS bf16*)(wl + 0 + t * 144 + ln * 2) = (bf16)(cvt_nat(at[t], 0.f) & 0xffffu);
;                     *(LAS bf16*)(wl + 2304 + t * 144 + ln * 2) = (bf16)((t & 1) ? (bhp[t >> 1] >> 16) : (bhp[t >> 1] & 0xffffu));
;                     *(LAS bf16*)(wl + 4608 + t * 144 + ln * 2) = (bf16)((t & 1) ? (khp[t >> 1] >> 16) : (khp[t >> 1] & 0xffffu));
;                     *(LAS bf16*)(wl + 6912 + t * 144 + ln * 2) = (bf16)(cvt_nat(rt[t], 0.f) & 0xffffu);
;                 }
	v_mul_f32_e32 v53, v49, v103
	v_cvt_pk_bf16_f32 v52, v16, v17
	s_waitcnt vmcnt(5)
	v_lshlrev_b32_e32 v17, 16, v107
	s_waitcnt vmcnt(0)
	s_and_b32 s16, s1, 0x3ffff0
	s_lshl_b32 s16, s16, 10
	s_and_b32 s17, s38, 0x3c0
	s_or_b32 s16, s16, s17
	s_add_i32 s16, s16, 0x100000
	s_lshl_b32 s17, s16, 1
	v_and_b32_e32 v240, 15, v0
	v_lshlrev_b32_e32 v240, 11, v240
	buffer_load_dword v241, v240, s[48:51], s17 offen
	buffer_load_dword v242, v240, s[28:31], s17 offen
	buffer_load_dword v243, v240, s[20:23], s17 offen
	buffer_load_dword v244, v240, s[24:27], s17 offen
	s_lshl_b32 s17, s16, 2
	v_lshlrev_b32_e32 v245, 1, v240
	v_and_b32_e32 v246, 16, v0
	v_lshl_add_u32 v245, v246, 3, v245
	buffer_load_dword v246, v245, s[44:47], s17 offen
	v_lshlrev_b32_e32 v18, 16, v112
	v_mul_f32_e32 v55, v53, v108
	v_lshlrev_b32_e32 v78, 16, v51
	v_cvt_pk_bf16_f32 v51, v24, v25
	v_rcp_f32_e32 v16, v53
	v_mul_f32_e32 v62, v53, v17
	v_rcp_f32_e32 v17, v55
	v_mul_f32_e32 v58, v55, v18
	v_lshlrev_b32_e32 v19, 16, v109
	v_lshlrev_b32_e32 v18, 16, v104
	v_lshlrev_b32_e32 v25, 16, v110
	v_lshlrev_b32_e32 v24, 16, v105
	v_mul_f32_e64 v50, v49, -v24
	v_mul_f32_e64 v54, v53, -v25
	v_pk_mul_f32 v[24:25], v[18:19], v[24:25]
	v_pk_add_f32 v[18:19], v[18:19], -1.0 op_sel_hi:[1,0]
	v_lshlrev_b32_e32 v21, 16, v111
	v_lshlrev_b32_e32 v20, 16, v106
	v_pk_fma_f32 v[18:19], v[2:3], v[18:19], 1.0 op_sel_hi:[0,1,0]
	v_pk_mul_f32 v[18:19], v[18:19], v[20:21]
	v_pk_mul_f32 v[24:25], v[24:25], v[16:17]
	v_pk_mul_f32 v[16:17], v[16:17], v[18:19]
	v_cvt_pk_bf16_f32 v2, v24, v25
	v_cvt_pk_bf16_f32 v20, v16, v17
	v_and_b32_e32 v16, 8, v0
	v_cmp_eq_u32_e64 s[16:17], 0, v16
	v_mov_b32_e32 v21, 0x1000
	s_and_b32 s81, s36, 0xffff
	s_mov_b32 s80, s33
	v_cndmask_b32_e64 v17, v33, v13, s[16:17]
	v_cndmask_b32_e64 v18, v51, v11, s[16:17]
	v_cndmask_b32_e64 v19, v2, v15, s[16:17]
	v_cndmask_b32_e64 v16, v23, v5, s[16:17]
	v_lshl_add_u32 v21, v0, 5, v21
	buffer_store_dwordx4 v[16:19], v21, s[80:83], 0 offen
	v_mul_f32_e32 v113, v84, v83
	v_mul_f32_e64 v34, v84, -v12
	v_cndmask_b32_e64 v17, v13, v33, s[16:17]
	v_cndmask_b32_e64 v18, v11, v51, s[16:17]
	v_cndmask_b32_e64 v19, v15, v2, s[16:17]
	v_cndmask_b32_e64 v16, v5, v23, s[16:17]
	buffer_store_dwordx4 v[16:19], v21, s[80:83], 0 offen offset:16
	v_mul_f32_e32 v27, v86, v85
	v_mul_f32_e64 v30, v86, -v10
	v_cndmask_b32_e64 v17, v48, v28, s[16:17]
	v_cndmask_b32_e64 v18, v52, v39, s[16:17]
	v_cndmask_b32_e64 v19, v20, v42, s[16:17]
	v_cndmask_b32_e64 v16, v44, v7, s[16:17]
	buffer_store_dwordx4 v[16:19], v21, s[80:83], 0 offen offset:2048
	v_mul_f32_e32 v29, v82, v81
	v_mul_f32_e64 v31, v82, -v14
	v_cndmask_b32_e64 v17, v28, v48, s[16:17]
	v_cndmask_b32_e64 v18, v39, v52, s[16:17]
	v_cndmask_b32_e64 v19, v42, v20, s[16:17]
	v_cndmask_b32_e64 v16, v7, v44, s[16:17]
	s_movk_i32 s16, 0x2c00
	buffer_store_dwordx4 v[16:19], v21, s[80:83], 0 offen offset:2064
	buffer_store_dword v55, v4, s[80:83], s16 offen
	v_add_u32_e32 v4, s3, v1
	v_cvt_pk_bf16_f32 v16, -v6, s0
	ds_write_b16 v4, v16
	ds_write_b16 v4, v5 offset:2304
	ds_write_b16 v4, v7 offset:4608
	v_cvt_pk_bf16_f32 v16, v70, s0
	ds_write_b16 v4, v16 offset:6912
	v_cvt_pk_bf16_f32 v16, v3, s0
	ds_write_b16 v4, v16 offset:144
	ds_write_b16_d16_hi v4, v5 offset:2448
	ds_write_b16_d16_hi v4, v7 offset:4752
	v_cvt_pk_bf16_f32 v5, v113, s0
	ds_write_b16 v4, v5 offset:7056
	v_cvt_pk_bf16_f32 v5, v34, s0
	ds_write_b16 v4, v5 offset:288
	ds_write_b16 v4, v13 offset:2592
	ds_write_b16 v4, v28 offset:4896
	v_cvt_pk_bf16_f32 v5, v88, s0
	ds_write_b16 v4, v5 offset:7200
	v_cvt_pk_bf16_f32 v5, v35, s0
	ds_write_b16 v4, v5 offset:432
	ds_write_b16_d16_hi v4, v13 offset:2736
	ds_write_b16_d16_hi v4, v28 offset:5040
	v_cvt_pk_bf16_f32 v5, v27, s0
	ds_write_b16 v4, v5 offset:7344
	v_cvt_pk_bf16_f32 v5, v30, s0
	ds_write_b16 v4, v5 offset:576
	ds_write_b16 v4, v11 offset:2880
	ds_write_b16 v4, v39 offset:5184
	v_cvt_pk_bf16_f32 v5, v87, s0
	ds_write_b16 v4, v5 offset:7488
	v_cvt_pk_bf16_f32 v5, v38, s0
	ds_write_b16 v4, v5 offset:720
	ds_write_b16_d16_hi v4, v11 offset:3024
	ds_write_b16_d16_hi v4, v39 offset:5328
	v_cvt_pk_bf16_f32 v5, v29, s0
	ds_write_b16 v4, v5 offset:7632
	v_cvt_pk_bf16_f32 v5, v31, s0
	ds_write_b16 v4, v5 offset:864
	ds_write_b16 v4, v15 offset:3168
	ds_write_b16 v4, v42 offset:5472
	v_cvt_pk_bf16_f32 v5, v80, s0
	v_mul_f32_e32 v41, v79, v78
	ds_write_b16 v4, v5 offset:7776
	v_cvt_pk_bf16_f32 v5, v47, s0
	v_mul_f32_e64 v43, v79, -v22
	ds_write_b16 v4, v5 offset:1008
	ds_write_b16_d16_hi v4, v15 offset:3312
	ds_write_b16_d16_hi v4, v42 offset:5616
	v_cvt_pk_bf16_f32 v5, v41, s0
	ds_write_b16 v4, v5 offset:7920
	v_cvt_pk_bf16_f32 v5, v43, s0
	ds_write_b16 v4, v5 offset:1152
	ds_write_b16 v4, v23 offset:3456
	ds_write_b16 v4, v44 offset:5760
	v_cvt_pk_bf16_f32 v5, v76, s0
	ds_write_b16 v4, v5 offset:8064
	v_cvt_pk_bf16_f32 v5, v26, s0
	v_mul_f32_e64 v45, v37, -v32
	ds_write_b16 v4, v5 offset:1296
	ds_write_b16_d16_hi v4, v23 offset:3600
	ds_write_b16_d16_hi v4, v44 offset:5904
	v_cvt_pk_bf16_f32 v5, v75, s0
	ds_write_b16 v4, v5 offset:8208
	v_cvt_pk_bf16_f32 v5, v45, s0
	ds_write_b16 v4, v5 offset:1440
	ds_write_b16 v4, v33 offset:3744
	ds_write_b16 v4, v48 offset:6048
	v_cvt_pk_bf16_f32 v5, v74, s0
	ds_write_b16 v4, v5 offset:8352
	v_cvt_pk_bf16_f32 v5, v36, s0
	ds_write_b16 v4, v5 offset:1584
	ds_write_b16_d16_hi v4, v33 offset:3888
	ds_write_b16_d16_hi v4, v48 offset:6192
	v_cvt_pk_bf16_f32 v5, v73, s0
	ds_write_b16 v4, v5 offset:8496
	v_cvt_pk_bf16_f32 v5, v40, s0
	ds_write_b16 v4, v5 offset:1728
	ds_write_b16 v4, v51 offset:4032
	ds_write_b16 v4, v52 offset:6336
	v_cvt_pk_bf16_f32 v5, v72, s0
	ds_write_b16 v4, v5 offset:8640
	v_cvt_pk_bf16_f32 v5, v46, s0
	ds_write_b16 v4, v5 offset:1872
	ds_write_b16_d16_hi v4, v51 offset:4176
	ds_write_b16_d16_hi v4, v52 offset:6480
	v_cvt_pk_bf16_f32 v5, v71, s0
	ds_write_b16 v4, v5 offset:8784
	v_cvt_pk_bf16_f32 v5, v50, s0
	ds_write_b16 v4, v5 offset:2016
	ds_write_b16 v4, v2 offset:4320
	ds_write_b16 v4, v20 offset:6624
	v_cvt_pk_bf16_f32 v5, v62, s0
	ds_write_b16 v4, v5 offset:8928
	v_cvt_pk_bf16_f32 v5, v54, s0
	ds_write_b16 v4, v5 offset:2160
	ds_write_b16_d16_hi v4, v2 offset:4464
	ds_write_b16_d16_hi v4, v20 offset:6768
	v_cvt_pk_bf16_f32 v2, v58, s0
	ds_write_b16 v4, v2 offset:9072
	s_waitcnt lgkmcnt(0)
; #define LAS __attribute__((address_space(3)))
; __global__ void __launch_bounds__(NWAVES * 64, 2) mk_fwd(Args args) {
;     ...
;                 LDS_WAIT(); asm volatile("" ::: "memory");
;                 {
;                     pg8::bf16x8 Aop[2], Bop[2], Kop[2], Rop[2];
; #pragma unroll
;                     for (int m = 0; m < 2; ++m) { const int o = c16 * 144 + 64 * m + 16 * g4;
;                         Aop[m] = *(const LAS pg8::bf16x8*)(wl + 0 + o); Bop[m] = *(const LAS pg8::bf16x8*)(wl + 2304 + o); Kop[m] = *(const LAS pg8::bf16x8*)(wl + 4608 + o); Rop[m] = *(const LAS pg8::bf16x8*)(wl + 6912 + o); }
;                     f32x4 nba = {0.f, 0.f, 0.f, 0.f}, nka = nba, nbr = nba, nkr = nba;
; #pragma unroll
;                     for (int m = 0; m < 2; ++m) {
;                         nba = __builtin_amdgcn_mfma_f32_16x16x32_bf16(Aop[m], Bop[m], nba, 0, 0, 0); nka = __builtin_amdgcn_mfma_f32_16x16x32_bf16(Aop[m], Kop[m], nka, 0, 0, 0);
;                         nbr = __builtin_amdgcn_mfma_f32_16x16x32_bf16(Rop[m], Bop[m], nbr, 0, 0, 0); nkr = __builtin_amdgcn_mfma_f32_16x16x32_bf16(Rop[m], Kop[m], nkr, 0, 0, 0);
;                     }
; #pragma unroll
;                     for (int e = 0; e < 4; ++e) { const int t = 4 * g4 + e; const bool lt = c16 < t, le = c16 <= t; LAS float* np = (LAS float*)(wl + 9216) + t * 16 + c16;
;                         np[0] = lt ? nba[e] : 0.f; np[256] = lt ? nka[e] : 0.f; np[512] = le ? nbr[e] : 0.f; np[768] = le ? nkr[e] : 0.f; }
;                 }
;                 LDS_WAIT(); asm volatile("" ::: "memory");
;                 float a2[16], a4[16];
;                 {
;                     const LAS float* NB_ = (const LAS float*)(wl + 9216);
;                     f32x4 nc[4], nn[4]; float rc = NB_[256 + c16], rn = 0.f;
; #pragma unroll
;                     for (int q = 0; q < 4; ++q) { nc[q] = (f32x4){0.f, 0.f, 0.f, 0.f}; nn[q] = nc[q]; }
; #pragma unroll
;                     for (int t = 0; t < 16; ++t) {
;                         if (t < 15) { rn = NB_[256 + (t + 1) * 16 + c16];
; #pragma unroll
;                             for (int sq = 0; sq < (t + 4) / 4; ++sq) nn[sq] = *(const LAS f32x4*)(NB_ + (t + 1) * 16 + 4 * sq); }
;                         float x1 = at[t], x2 = rc;
; #pragma unroll
;                         for (int sq = 0; sq < (t + 3) / 4; ++sq) {
; #pragma unroll
	ds_read_b128 v[16:19], v65
	ds_read_b128 v[28:31], v65 offset:2304
	ds_read_b128 v[42:45], v65 offset:64
	ds_read_b128 v[90:93], v65 offset:2368
	ds_read_b128 v[98:101], v65 offset:4608
	ds_read_b128 v[102:105], v65 offset:4672
	ds_read_b128 v[106:109], v65 offset:6912
	ds_read_b128 v[110:113], v65 offset:6976
	s_waitcnt lgkmcnt(6)
	v_mfma_f32_16x16x32_bf16 v[94:97], v[16:19], v[28:31], 0
	v_mov_b32_e32 v77, s3
	v_add_u32_e32 v89, 0x3000, v64
	s_movk_i32 s16, 0x800
	s_waitcnt lgkmcnt(3)
	v_mfma_f32_16x16x32_bf16 v[16:19], v[16:19], v[98:101], 0
	s_waitcnt lgkmcnt(1)
	v_mfma_f32_16x16x32_bf16 v[28:31], v[106:109], v[28:31], 0
	v_mfma_f32_16x16x32_bf16 v[98:101], v[106:109], v[98:101], 0
	v_mfma_f32_16x16x32_bf16 v[94:97], v[42:45], v[90:93], v[94:97]
	v_mfma_f32_16x16x32_bf16 v[16:19], v[42:45], v[102:105], v[16:19]
	s_waitcnt lgkmcnt(0)
	v_mfma_f32_16x16x32_bf16 v[28:31], v[110:113], v[90:93], v[28:31]
	s_nop 4
	v_cndmask_b32_e32 v2, 0, v94, vcc
	v_cndmask_b32_e32 v4, 0, v16, vcc
	ds_write2st64_b32 v66, v2, v4 offset0:36 offset1:40
	v_mfma_f32_16x16x32_bf16 v[42:45], v[110:113], v[102:105], v[98:101]
	v_cndmask_b32_e64 v2, v28, 0, s[4:5]
	s_nop 6
	v_cndmask_b32_e64 v4, v42, 0, s[4:5]
	ds_write2st64_b32 v66, v2, v4 offset0:44 offset1:48
	v_cndmask_b32_e64 v2, v95, 0, s[4:5]
	v_cndmask_b32_e64 v4, v17, 0, s[4:5]
	ds_write2st64_b32 v67, v2, v4 offset0:36 offset1:40
	v_cndmask_b32_e64 v2, v29, 0, s[6:7]
	v_cndmask_b32_e64 v4, v43, 0, s[6:7]
	ds_write2st64_b32 v67, v2, v4 offset0:44 offset1:48
	v_cndmask_b32_e64 v2, 0, v96, s[8:9]
	v_cndmask_b32_e64 v4, 0, v18, s[8:9]
	ds_write2st64_b32 v68, v2, v4 offset0:36 offset1:40
	v_cndmask_b32_e64 v2, v30, 0, s[10:11]
	v_cndmask_b32_e64 v4, v44, 0, s[10:11]
	ds_write2st64_b32 v68, v2, v4 offset0:44 offset1:48
	v_cndmask_b32_e64 v2, 0, v97, s[12:13]
	v_cndmask_b32_e64 v4, 0, v19, s[12:13]
	ds_write2st64_b32 v69, v2, v4 offset0:36 offset1:40
	v_cndmask_b32_e64 v2, v31, 0, s[14:15]
	v_cndmask_b32_e64 v4, v45, 0, s[14:15]
	ds_write2st64_b32 v69, v2, v4 offset0:44 offset1:48
	s_waitcnt lgkmcnt(0)
	v_add_u32_e32 v2, 0x2800, v64
	ds_read2_b32 v[4:5], v2 offset1:16
	ds_read_b128 v[16:19], v77 offset:9280
	v_xor_b32_e32 v2, 0x80000000, v6
	s_waitcnt lgkmcnt(1)
	ds_read_b32 v11, v64 offset:10368
	ds_read_b64 v[6:7], v77 offset:9344
	s_waitcnt lgkmcnt(2)
	v_fmac_f32_e32 v3, v16, v2
	v_fmac_f32_e32 v5, v16, v4
	ds_read_b32 v15, v64 offset:10432
	ds_read_b128 v[16:19], v77 offset:9408
	s_waitcnt lgkmcnt(2)
	v_pk_mul_f32 v[20:21], v[6:7], v[2:3]
	v_pk_mul_f32 v[6:7], v[6:7], v[4:5]
	v_fma_f32 v12, v84, -v12, v20
	v_add_f32_e32 v6, v11, v6
	s_waitcnt lgkmcnt(0)
	v_add_f32_e32 v19, v12, v21
	v_add_f32_e32 v7, v6, v7
	v_mov_b32_e32 v12, v17
	v_mov_b32_e32 v13, v18
	v_mov_b32_e32 v18, v3
	ds_read_b32 v20, v64 offset:10496
	ds_read_b128 v[28:31], v77 offset:9472
	v_fmac_f32_e32 v35, v16, v2
	v_fmac_f32_e32 v15, v16, v4
	v_pk_mul_f32 v[16:17], v[12:13], v[18:19]
	s_nop 0
	v_add_f32_e32 v6, v35, v16
	v_add_f32_e32 v21, v6, v17
	v_mov_b32_e32 v6, v5
	v_pk_mul_f32 v[12:13], v[12:13], v[6:7]
	s_waitcnt lgkmcnt(0)
	v_pk_mul_f32 v[16:17], v[28:29], v[2:3]
	v_add_f32_e32 v11, v15, v12
	v_add_f32_e32 v11, v11, v13
	v_fma_f32 v10, v86, -v10, v16
	ds_read_b32 v15, v64 offset:10560
	ds_read_b128 v[42:45], v77 offset:9536
	ds_read_b64 v[12:13], v77 offset:9552
	v_add_f32_e32 v10, v10, v17
	v_pk_mul_f32 v[16:17], v[28:29], v[4:5]
	s_waitcnt lgkmcnt(1)
	v_mov_b32_e32 v28, v43
	s_waitcnt lgkmcnt(0)
	v_add_f32_e32 v13, v20, v16
	v_mov_b32_e32 v20, v19
	v_add_f32_e32 v13, v13, v17
	v_pk_mul_f32 v[16:17], v[30:31], v[20:21]
	v_mov_b32_e32 v29, v44
	v_add_f32_e32 v10, v10, v16
	v_add_f32_e32 v25, v10, v17
	v_mov_b32_e32 v10, v7
	v_pk_mul_f32 v[16:17], v[30:31], v[10:11]
	v_fmac_f32_e32 v38, v42, v2
	v_pk_mul_f32 v[30:31], v[28:29], v[18:19]
	v_add_f32_e32 v13, v13, v16
	v_fmac_f32_e32 v15, v42, v4
	v_add_f32_e32 v24, v38, v30
	v_pk_mul_f32 v[28:29], v[28:29], v[6:7]
	v_add_f32_e32 v13, v13, v17
	v_add_f32_e32 v27, v24, v31
	v_add_f32_e32 v15, v15, v28
	v_mov_b32_e32 v30, v45
	v_mov_b32_e32 v31, v12
	v_mov_b32_e32 v24, v21
	v_add_f32_e32 v15, v15, v29
	v_pk_mul_f32 v[28:29], v[30:31], v[24:25]
	ds_read_b32 v23, v64 offset:10624
	ds_read_b128 v[90:93], v77 offset:9600
	ds_read_b64 v[16:17], v77 offset:9616
	v_add_f32_e32 v12, v27, v28
	v_add_f32_e32 v29, v12, v29
	v_mov_b32_e32 v12, v11
	v_pk_mul_f32 v[30:31], v[30:31], v[12:13]
	v_mov_b32_e32 v28, v25
	v_add_f32_e32 v15, v15, v30
	v_add_f32_e32 v15, v15, v31
	s_waitcnt lgkmcnt(1)
	v_pk_mul_f32 v[30:31], v[90:91], v[2:3]
	ds_read_b32 v27, v64 offset:10688
	ds_read_b128 v[42:45], v77 offset:9664
	ds_read_b128 v[94:97], v77 offset:9680
	v_fma_f32 v14, v82, -v14, v30
	v_add_f32_e32 v14, v14, v31
	v_pk_mul_f32 v[30:31], v[90:91], v[4:5]
	s_waitcnt lgkmcnt(1)
	v_mov_b32_e32 v34, v43
	v_add_f32_e32 v23, v23, v30
	v_add_f32_e32 v23, v23, v31
	v_pk_mul_f32 v[30:31], v[92:93], v[20:21]
	v_mov_b32_e32 v35, v44
	v_add_f32_e32 v14, v14, v30
	v_add_f32_e32 v14, v14, v31
	v_pk_mul_f32 v[30:31], v[92:93], v[10:11]
	v_fmac_f32_e32 v27, v42, v4
	v_add_f32_e32 v23, v23, v30
	v_add_f32_e32 v23, v23, v31
	v_pk_mul_f32 v[30:31], v[16:17], v[28:29]
	v_pk_mul_f32 v[38:39], v[34:35], v[18:19]
	v_add_f32_e32 v14, v14, v30
	v_add_f32_e32 v31, v14, v31
	v_mov_b32_e32 v14, v13
	v_pk_mul_f32 v[16:17], v[16:17], v[14:15]
	v_pk_mul_f32 v[34:35], v[34:35], v[6:7]
	v_add_f32_e32 v16, v23, v16
	v_fmac_f32_e32 v47, v42, v2
	v_add_f32_e32 v23, v27, v34
	v_add_f32_e32 v17, v16, v17
	v_add_f32_e32 v16, v47, v38
	v_add_f32_e32 v23, v23, v35
	v_mov_b32_e32 v34, v45
	s_waitcnt lgkmcnt(0)
; #define LAS __attribute__((address_space(3)))
; __global__ void __launch_bounds__(NWAVES * 64, 2) mk_fwd(Args args) {
;     ...
; #pragma unroll
;                     for (int t = 0; t < 16; ++t) {
;                         if (t < 15) { rn = NB_[256 + (t + 1) * 16 + c16];
; #pragma unroll
;                             for (int sq = 0; sq < (t + 4) / 4; ++sq) nn[sq] = *(const LAS f32x4*)(NB_ + (t + 1) * 16 + 4 * sq); }
;                         float x1 = at[t], x2 = rc;
; #pragma unroll
;                         for (int sq = 0; sq < (t + 3) / 4; ++sq) {
; #pragma unroll
;                             for (int e = 0; e < 4; ++e) if (4 * sq + e < t) { x1 += nc[sq][e] * at[4 * sq + e]; x2 += nc[sq][e] * a2[4 * sq + e]; } }
;                         asm volatile("" : "+v"(x1), "+v"(x2) :: "memory");
;                         at[t] = x1; a2[t] = x2; rc = rn;
; #pragma unroll
;                         for (int q = 0; q < 4; ++q) nc[q] = nn[q];
;                     }
	v_mov_b32_e32 v35, v94
	v_add_f32_e32 v16, v16, v39
	v_pk_mul_f32 v[38:39], v[34:35], v[24:25]
	ds_read_b32 v33, v64 offset:10752
	ds_read_b128 v[90:93], v77 offset:9728
	ds_read_b128 v[98:101], v77 offset:9744
	v_add_f32_e32 v16, v16, v38
	v_pk_mul_f32 v[34:35], v[34:35], v[12:13]
	v_add_f32_e32 v16, v16, v39
	v_add_f32_e32 v23, v23, v34
	v_mov_b32_e32 v38, v95
	v_mov_b32_e32 v39, v96
	v_mov_b32_e32 v30, v29
	v_add_f32_e32 v23, v23, v35
	v_pk_mul_f32 v[34:35], v[38:39], v[30:31]
	s_waitcnt lgkmcnt(1)
	v_pk_mul_f32 v[48:49], v[90:91], v[2:3]
	v_add_f32_e32 v16, v16, v34
	v_add_f32_e32 v35, v16, v35
	v_mov_b32_e32 v16, v15
	v_pk_mul_f32 v[38:39], v[38:39], v[16:17]
	v_fma_f32 v22, v79, -v22, v48
	v_add_f32_e32 v23, v23, v38
	v_add_f32_e32 v22, v22, v49
	v_pk_mul_f32 v[48:49], v[90:91], v[4:5]
	v_add_f32_e32 v23, v23, v39
	v_add_f32_e32 v27, v33, v48
	v_add_f32_e32 v27, v27, v49
	v_pk_mul_f32 v[48:49], v[92:93], v[20:21]
	ds_read_b32 v41, v64 offset:10816
	ds_read_b128 v[42:45], v77 offset:9792
	ds_read_b128 v[94:97], v77 offset:9808
	ds_read_b64 v[38:39], v77 offset:9824
	v_add_f32_e32 v22, v22, v48
	v_add_f32_e32 v22, v22, v49
	v_pk_mul_f32 v[48:49], v[92:93], v[10:11]
	s_waitcnt lgkmcnt(2)
	v_fmac_f32_e32 v26, v42, v2
	v_add_f32_e32 v27, v27, v48
	v_add_f32_e32 v27, v27, v49
	v_pk_mul_f32 v[48:49], v[98:99], v[28:29]
	v_fmac_f32_e32 v41, v42, v4
	v_mov_b32_e32 v42, v43
	v_mov_b32_e32 v43, v44
	v_add_f32_e32 v22, v22, v48
	v_pk_mul_f32 v[52:53], v[42:43], v[18:19]
	v_pk_mul_f32 v[42:43], v[42:43], v[6:7]
	v_add_f32_e32 v22, v22, v49
	v_pk_mul_f32 v[48:49], v[98:99], v[14:15]
	v_add_f32_e32 v33, v41, v42
	v_add_f32_e32 v27, v27, v48
	v_mov_b32_e32 v34, v31
	v_add_f32_e32 v33, v33, v43
	v_mov_b32_e32 v42, v45
	s_waitcnt lgkmcnt(1)
	v_mov_b32_e32 v43, v94
	v_add_f32_e32 v27, v27, v49
	v_pk_mul_f32 v[48:49], v[100:101], v[34:35]
	v_add_f32_e32 v26, v26, v52
	v_pk_mul_f32 v[44:45], v[42:43], v[24:25]
	v_pk_mul_f32 v[42:43], v[42:43], v[12:13]
	v_add_f32_e32 v22, v22, v48
	v_add_f32_e32 v26, v26, v53
	v_add_f32_e32 v33, v33, v42
	s_waitcnt lgkmcnt(0)
	v_add_f32_e32 v39, v22, v49
	v_mov_b32_e32 v22, v17
	v_add_f32_e32 v26, v26, v44
	v_add_f32_e32 v33, v33, v43
	v_mov_b32_e32 v42, v95
	v_mov_b32_e32 v43, v96
	v_pk_mul_f32 v[48:49], v[100:101], v[22:23]
	v_add_f32_e32 v26, v26, v45
	v_pk_mul_f32 v[44:45], v[42:43], v[30:31]
	v_add_f32_e32 v27, v27, v48
	v_add_f32_e32 v26, v26, v44
	v_pk_mul_f32 v[42:43], v[42:43], v[16:17]
	v_add_f32_e32 v27, v27, v49
	v_add_f32_e32 v26, v26, v45
	v_add_f32_e32 v33, v33, v42
	v_mov_b32_e32 v44, v97
	v_mov_b32_e32 v45, v38
	v_mov_b32_e32 v38, v35
	v_add_f32_e32 v33, v33, v43
	v_pk_mul_f32 v[42:43], v[44:45], v[38:39]
	ds_read_b32 v47, v64 offset:10880
	ds_read_b128 v[90:93], v77 offset:9856
	ds_read_b128 v[98:101], v77 offset:9872
	ds_read_b64 v[48:49], v77 offset:9888
	v_add_f32_e32 v26, v26, v42
	v_add_f32_e32 v43, v26, v43
	v_mov_b32_e32 v26, v23
	v_pk_mul_f32 v[44:45], v[44:45], v[26:27]
	v_mov_b32_e32 v42, v39
	v_add_f32_e32 v33, v33, v44
	v_add_f32_e32 v33, v33, v45
	s_waitcnt lgkmcnt(2)
	v_pk_mul_f32 v[44:45], v[90:91], v[2:3]
	ds_read_b32 v41, v64 offset:10944
	ds_read_b128 v[94:97], v77 offset:9920
	ds_read_b128 v[102:105], v77 offset:9936
	ds_read_b128 v[106:109], v77 offset:9952
	v_fma_f32 v32, v37, -v32, v44
	v_add_f32_e32 v32, v32, v45
	v_pk_mul_f32 v[44:45], v[90:91], v[4:5]
	s_waitcnt lgkmcnt(2)
	v_fmac_f32_e32 v41, v94, v4
	v_add_f32_e32 v37, v47, v44
	v_add_f32_e32 v37, v37, v45
	v_pk_mul_f32 v[44:45], v[92:93], v[20:21]
	v_fmac_f32_e32 v36, v94, v2
	v_add_f32_e32 v32, v32, v44
	v_add_f32_e32 v32, v32, v45
	v_pk_mul_f32 v[44:45], v[92:93], v[10:11]
	s_nop 0
	v_add_f32_e32 v37, v37, v44
	v_add_f32_e32 v37, v37, v45
	v_pk_mul_f32 v[44:45], v[98:99], v[28:29]
	s_nop 0
	v_add_f32_e32 v32, v32, v44
	v_add_f32_e32 v32, v32, v45
	v_pk_mul_f32 v[44:45], v[98:99], v[14:15]
	s_nop 0
	v_add_f32_e32 v37, v37, v44
	v_add_f32_e32 v37, v37, v45
	v_pk_mul_f32 v[44:45], v[100:101], v[34:35]
	s_nop 0
	v_add_f32_e32 v32, v32, v44
	v_add_f32_e32 v32, v32, v45
	v_pk_mul_f32 v[44:45], v[100:101], v[22:23]
	s_nop 0
	v_add_f32_e32 v37, v37, v44
	v_add_f32_e32 v37, v37, v45
	v_pk_mul_f32 v[44:45], v[48:49], v[42:43]
	s_nop 0
	v_add_f32_e32 v32, v32, v44
	v_add_f32_e32 v45, v32, v45
	v_mov_b32_e32 v32, v27
	v_pk_mul_f32 v[48:49], v[48:49], v[32:33]
	v_mov_b32_e32 v44, v43
	v_add_f32_e32 v37, v37, v48
	v_add_f32_e32 v37, v37, v49
	ds_read_b32 v47, v64 offset:11008
	ds_read_b128 v[90:93], v77 offset:9984
	ds_read_b128 v[98:101], v77 offset:10000
	ds_read_b128 v[110:113], v77 offset:10016
	v_mov_b32_e32 v48, v95
	v_mov_b32_e32 v49, v96
	v_pk_mul_f32 v[52:53], v[48:49], v[18:19]
	v_pk_mul_f32 v[48:49], v[48:49], v[6:7]
	s_waitcnt lgkmcnt(2)
	v_fmac_f32_e32 v40, v90, v2
	v_add_f32_e32 v41, v41, v48
	v_add_f32_e32 v36, v36, v52
	v_add_f32_e32 v41, v41, v49
	v_mov_b32_e32 v48, v97
	v_mov_b32_e32 v49, v102
	v_fmac_f32_e32 v40, v91, v3
	v_pk_mul_f32 v[56:57], v[92:93], v[20:21]
	v_add_f32_e32 v36, v36, v53
	v_pk_mul_f32 v[52:53], v[48:49], v[24:25]
	v_pk_mul_f32 v[48:49], v[48:49], v[12:13]
	v_fmac_f32_e32 v47, v90, v4
	v_add_f32_e32 v40, v40, v56
	v_add_f32_e32 v41, v41, v48
	v_fmac_f32_e32 v47, v91, v5
	v_add_f32_e32 v40, v40, v57
	v_pk_mul_f32 v[56:57], v[92:93], v[10:11]
	v_add_f32_e32 v36, v36, v52
	v_add_f32_e32 v41, v41, v49
	v_mov_b32_e32 v48, v103
	v_mov_b32_e32 v49, v104
	v_add_f32_e32 v47, v47, v56
	v_add_f32_e32 v36, v36, v53
	v_pk_mul_f32 v[52:53], v[48:49], v[30:31]
	v_pk_mul_f32 v[48:49], v[48:49], v[16:17]
	v_add_f32_e32 v47, v47, v57
	s_waitcnt lgkmcnt(1)
; #define LAS __attribute__((address_space(3)))
; __global__ void __launch_bounds__(NWAVES * 64, 2) mk_fwd(Args args) {
;     ...
; #pragma unroll
;                     for (int t = 0; t < 16; ++t) {
;                         if (t < 15) { rn = NB_[256 + (t + 1) * 16 + c16];
; #pragma unroll
;                             for (int sq = 0; sq < (t + 4) / 4; ++sq) nn[sq] = *(const LAS f32x4*)(NB_ + (t + 1) * 16 + 4 * sq); }
;                         float x1 = at[t], x2 = rc;
; #pragma unroll
;                         for (int sq = 0; sq < (t + 3) / 4; ++sq) {
; #pragma unroll
;                             for (int e = 0; e < 4; ++e) if (4 * sq + e < t) { x1 += nc[sq][e] * at[4 * sq + e]; x2 += nc[sq][e] * a2[4 * sq + e]; } }
;                         asm volatile("" : "+v"(x1), "+v"(x2) :: "memory");
;                         at[t] = x1; a2[t] = x2; rc = rn;
; #pragma unroll
;                         for (int q = 0; q < 4; ++q) nc[q] = nn[q];
;                     }
	v_pk_mul_f32 v[56:57], v[98:99], v[28:29]
	v_add_f32_e32 v41, v41, v48
	v_add_f32_e32 v40, v40, v56
	v_add_f32_e32 v36, v36, v52
	v_add_f32_e32 v41, v41, v49
	v_mov_b32_e32 v48, v105
	v_mov_b32_e32 v49, v106
	v_add_f32_e32 v40, v40, v57
	v_pk_mul_f32 v[56:57], v[98:99], v[14:15]
	v_add_f32_e32 v36, v36, v53
	v_pk_mul_f32 v[52:53], v[48:49], v[38:39]
	v_add_f32_e32 v47, v47, v56
	v_add_f32_e32 v36, v36, v52
	v_pk_mul_f32 v[48:49], v[48:49], v[26:27]
	v_add_f32_e32 v47, v47, v57
	v_pk_mul_f32 v[56:57], v[100:101], v[34:35]
	v_add_f32_e32 v36, v36, v53
	v_add_f32_e32 v41, v41, v48
	v_mov_b32_e32 v52, v107
	v_mov_b32_e32 v53, v108
	v_add_f32_e32 v40, v40, v56
	v_add_f32_e32 v41, v41, v49
	v_pk_mul_f32 v[48:49], v[52:53], v[44:45]
	v_add_f32_e32 v40, v40, v57
	v_pk_mul_f32 v[56:57], v[100:101], v[22:23]
	v_add_f32_e32 v36, v36, v48
	v_add_f32_e32 v47, v47, v56
	v_add_f32_e32 v49, v36, v49
	v_mov_b32_e32 v36, v33
	v_add_f32_e32 v47, v47, v57
	s_waitcnt lgkmcnt(0)
	v_pk_mul_f32 v[56:57], v[110:111], v[42:43]
	v_pk_mul_f32 v[52:53], v[52:53], v[36:37]
	v_add_f32_e32 v40, v40, v56
	v_add_f32_e32 v41, v41, v52
	v_add_f32_e32 v40, v40, v57
	v_pk_mul_f32 v[56:57], v[110:111], v[32:33]
	v_add_f32_e32 v41, v41, v53
	v_add_f32_e32 v47, v47, v56
	v_mov_b32_e32 v48, v45
	v_add_f32_e32 v47, v47, v57
	v_pk_mul_f32 v[56:57], v[112:113], v[48:49]
	ds_read_b32 v51, v64 offset:11072
	ds_read_b128 v[94:97], v77 offset:10048
	ds_read_b128 v[102:105], v77 offset:10064
	ds_read_b128 v[106:109], v77 offset:10080
	ds_read_b64 v[52:53], v77 offset:10096
	v_add_f32_e32 v40, v40, v56
	s_waitcnt lgkmcnt(0)
	v_add_f32_e32 v53, v40, v57
	v_mov_b32_e32 v40, v37
	v_pk_mul_f32 v[56:57], v[112:113], v[40:41]
	v_fmac_f32_e32 v51, v94, v4
	v_add_f32_e32 v47, v47, v56
	v_add_f32_e32 v47, v47, v57
	v_fmac_f32_e32 v46, v94, v2
	v_fmac_f32_e32 v51, v95, v5
	v_mov_b32_e32 v56, v97
	v_mov_b32_e32 v57, v102
	v_fmac_f32_e32 v46, v95, v3
	v_fmac_f32_e32 v51, v96, v7
	v_pk_mul_f32 v[60:61], v[56:57], v[24:25]
	v_pk_mul_f32 v[56:57], v[56:57], v[12:13]
	v_fmac_f32_e32 v46, v96, v19
	v_add_f32_e32 v51, v51, v56
	v_add_f32_e32 v46, v46, v60
	v_add_f32_e32 v51, v51, v57
	v_mov_b32_e32 v56, v103
	v_mov_b32_e32 v57, v104
	v_add_f32_e32 v46, v46, v61
	v_pk_mul_f32 v[60:61], v[56:57], v[30:31]
	v_pk_mul_f32 v[56:57], v[56:57], v[16:17]
	v_add_f32_e32 v46, v46, v60
	v_add_f32_e32 v51, v51, v56
	v_add_f32_e32 v51, v51, v57
	v_mov_b32_e32 v56, v105
	v_mov_b32_e32 v57, v106
	v_add_f32_e32 v46, v46, v61
	v_pk_mul_f32 v[60:61], v[56:57], v[38:39]
	v_pk_mul_f32 v[56:57], v[56:57], v[26:27]
	v_add_f32_e32 v46, v46, v60
	v_add_f32_e32 v51, v51, v56
	v_add_f32_e32 v51, v51, v57
	v_mov_b32_e32 v56, v107
	v_mov_b32_e32 v57, v108
	v_add_f32_e32 v46, v46, v61
	v_pk_mul_f32 v[60:61], v[56:57], v[44:45]
	v_pk_mul_f32 v[56:57], v[56:57], v[36:37]
	v_add_f32_e32 v46, v46, v60
	v_add_f32_e32 v46, v46, v61
	v_add_f32_e32 v51, v51, v56
	v_mov_b32_e32 v60, v109
	v_mov_b32_e32 v61, v52
	v_mov_b32_e32 v52, v49
	ds_read_b32 v55, v64 offset:11136
	ds_read_b128 v[90:93], v77 offset:10112
	ds_read_b128 v[98:101], v77 offset:10128
	ds_read_b128 v[110:113], v77 offset:10144
	ds_read_b64 v[118:119], v77 offset:10160
	v_add_f32_e32 v51, v51, v57
	v_pk_mul_f32 v[56:57], v[60:61], v[52:53]
	s_waitcnt lgkmcnt(3)
	v_fmac_f32_e32 v50, v90, v2
	v_add_f32_e32 v46, v46, v56
	v_add_f32_e32 v57, v46, v57
	v_mov_b32_e32 v46, v41
	v_pk_mul_f32 v[60:61], v[60:61], v[46:47]
	v_fmac_f32_e32 v50, v91, v3
	v_add_f32_e32 v51, v51, v60
	v_fmac_f32_e32 v55, v90, v4
	v_fmac_f32_e32 v50, v92, v19
	v_add_f32_e32 v51, v51, v61
	v_fmac_f32_e32 v55, v91, v5
	v_fmac_f32_e32 v50, v93, v21
	s_waitcnt lgkmcnt(2)
	v_pk_mul_f32 v[60:61], v[98:99], v[28:29]
	v_fmac_f32_e32 v55, v92, v7
	v_add_f32_e32 v50, v50, v60
	v_fmac_f32_e32 v55, v93, v11
	v_add_f32_e32 v50, v50, v61
	v_pk_mul_f32 v[60:61], v[98:99], v[14:15]
	v_mov_b32_e32 v56, v53
	v_add_f32_e32 v55, v55, v60
	v_add_f32_e32 v55, v55, v61
	v_pk_mul_f32 v[60:61], v[100:101], v[34:35]
	ds_read_b32 v59, v64 offset:11200
	ds_read_b128 v[94:97], v77 offset:10176
	ds_read_b128 v[102:105], v77 offset:10192
	ds_read_b128 v[106:109], v77 offset:10208
	ds_read_b128 v[114:117], v77 offset:10224
	v_add_f32_e32 v50, v50, v60
	v_add_f32_e32 v50, v50, v61
	v_pk_mul_f32 v[60:61], v[100:101], v[22:23]
	s_waitcnt lgkmcnt(3)
	v_fmac_f32_e32 v59, v94, v4
	v_add_f32_e32 v55, v55, v60
	v_add_f32_e32 v55, v55, v61
	v_pk_mul_f32 v[60:61], v[110:111], v[42:43]
	v_fmac_f32_e32 v54, v94, v2
	v_add_f32_e32 v50, v50, v60
	v_add_f32_e32 v50, v50, v61
	v_pk_mul_f32 v[60:61], v[110:111], v[32:33]
	v_fmac_f32_e32 v59, v95, v5
	v_add_f32_e32 v55, v55, v60
	v_add_f32_e32 v55, v55, v61
	v_pk_mul_f32 v[60:61], v[112:113], v[48:49]
	v_fmac_f32_e32 v54, v95, v3
	v_add_f32_e32 v50, v50, v60
	v_add_f32_e32 v50, v50, v61
	v_pk_mul_f32 v[60:61], v[112:113], v[40:41]
	v_fmac_f32_e32 v59, v96, v7
	v_add_f32_e32 v55, v55, v60
	v_add_f32_e32 v55, v55, v61
	v_pk_mul_f32 v[60:61], v[118:119], v[56:57]
	v_fmac_f32_e32 v54, v96, v19
	v_add_f32_e32 v50, v50, v60
	v_add_f32_e32 v61, v50, v61
	v_mov_b32_e32 v50, v47
	v_pk_mul_f32 v[90:91], v[118:119], v[50:51]
	v_fmac_f32_e32 v59, v97, v11
	v_add_f32_e32 v55, v55, v90
	v_add_f32_e32 v55, v55, v91
	s_waitcnt lgkmcnt(2)
	v_mov_b32_e32 v90, v103
	v_mov_b32_e32 v91, v104
	v_fmac_f32_e32 v54, v97, v21
	v_fmac_f32_e32 v59, v102, v13
	v_pk_mul_f32 v[92:93], v[90:91], v[30:31]
	v_pk_mul_f32 v[90:91], v[90:91], v[16:17]
	v_fmac_f32_e32 v54, v102, v25
	v_add_f32_e32 v59, v59, v90
	v_add_f32_e32 v54, v54, v92
	v_add_f32_e32 v59, v59, v91
	v_mov_b32_e32 v90, v105
	s_waitcnt lgkmcnt(1)
; #define LAS __attribute__((address_space(3)))
; __global__ void __launch_bounds__(NWAVES * 64, 2) mk_fwd(Args args) {
;     ...
; #pragma unroll
;                     for (int t = 0; t < 16; ++t) {
;                         if (t < 15) { rn = NB_[256 + (t + 1) * 16 + c16];
; #pragma unroll
;                             for (int sq = 0; sq < (t + 4) / 4; ++sq) nn[sq] = *(const LAS f32x4*)(NB_ + (t + 1) * 16 + 4 * sq); }
;                         float x1 = at[t], x2 = rc;
; #pragma unroll
;                         for (int sq = 0; sq < (t + 3) / 4; ++sq) {
; #pragma unroll
;                             for (int e = 0; e < 4; ++e) if (4 * sq + e < t) { x1 += nc[sq][e] * at[4 * sq + e]; x2 += nc[sq][e] * a2[4 * sq + e]; } }
;                         asm volatile("" : "+v"(x1), "+v"(x2) :: "memory");
;                         at[t] = x1; a2[t] = x2; rc = rn;
; #pragma unroll
;                         for (int q = 0; q < 4; ++q) nc[q] = nn[q];
;                     }
;                     rc = NB_[768 + c16]; nc[0] = *(const LAS f32x4*)(NB_ + 512);
; #pragma unroll
;                     for (int t = 0; t < 16; ++t) {
;                         if (t < 15) { rn = NB_[768 + (t + 1) * 16 + c16];
; #pragma unroll
;                             for (int sq = 0; sq < (t + 5) / 4; ++sq) nn[sq] = *(const LAS f32x4*)(NB_ + 512 + (t + 1) * 16 + 4 * sq); }
;                         float x3 = rt[t], x4 = rc;
; #pragma unroll
;                         for (int sq = 0; sq < (t + 4) / 4; ++sq) {
; #pragma unroll
;                             for (int e = 0; e < 4; ++e) if (4 * sq + e <= t) { x3 += nc[sq][e] * at[4 * sq + e]; x4 += nc[sq][e] * a2[4 * sq + e]; } }
;                         asm volatile("" : "+v"(x3), "+v"(x4) :: "memory");
;                         rt[t] = x3; a4[t] = x4; rc = rn;
; #pragma unroll
;                         for (int q = 0; q < 4; ++q) nc[q] = nn[q];
;                     }
	v_mov_b32_e32 v91, v106
	v_add_f32_e32 v54, v54, v93
	v_pk_mul_f32 v[92:93], v[90:91], v[38:39]
	v_pk_mul_f32 v[90:91], v[90:91], v[26:27]
	v_add_f32_e32 v54, v54, v92
	v_add_f32_e32 v59, v59, v90
	v_add_f32_e32 v59, v59, v91
	v_mov_b32_e32 v90, v107
	v_mov_b32_e32 v91, v108
	v_add_f32_e32 v54, v54, v93
	v_pk_mul_f32 v[92:93], v[90:91], v[44:45]
	v_pk_mul_f32 v[90:91], v[90:91], v[36:37]
	v_add_f32_e32 v54, v54, v92
	v_add_f32_e32 v59, v59, v90
	v_add_f32_e32 v59, v59, v91
	v_mov_b32_e32 v90, v109
	s_waitcnt lgkmcnt(0)
	v_mov_b32_e32 v91, v114
	v_add_f32_e32 v54, v54, v93
	v_pk_mul_f32 v[92:93], v[90:91], v[52:53]
	v_pk_mul_f32 v[90:91], v[90:91], v[46:47]
	v_add_f32_e32 v54, v54, v92
	v_add_f32_e32 v59, v59, v90
	v_add_f32_e32 v59, v59, v91
	v_mov_b32_e32 v90, v115
	v_mov_b32_e32 v91, v116
	v_mov_b32_e32 v60, v57
	v_add_f32_e32 v54, v54, v93
	v_pk_mul_f32 v[92:93], v[90:91], v[60:61]
	s_nop 0
	v_add_f32_e32 v54, v54, v92
	v_add_f32_e32 v63, v54, v93
	v_mov_b32_e32 v54, v51
	v_pk_mul_f32 v[90:91], v[90:91], v[54:55]
	s_nop 0
	v_add_f32_e32 v59, v59, v90
	v_add_f32_e32 v59, v59, v91
	ds_read_b128 v[90:93], v77 offset:11264
	ds_read2_b32 v[96:97], v89 offset1:16
	ds_read_b64 v[98:99], v77 offset:11328
	s_waitcnt lgkmcnt(2)
	v_fmac_f32_e32 v70, v90, v2
	s_waitcnt lgkmcnt(1)
	v_fma_f32 v89, v90, v4, v96
	ds_read_b32 v100, v64 offset:12416
	ds_read_b128 v[92:95], v77 offset:11392
	s_waitcnt lgkmcnt(2)
	v_pk_mul_f32 v[90:91], v[98:99], v[2:3]
	v_pk_mul_f32 v[98:99], v[98:99], v[4:5]
	v_fma_f32 v83, v84, v83, v90
	v_add_f32_e32 v90, v83, v91
	v_add_f32_e32 v83, v97, v98
	v_add_f32_e32 v83, v83, v99
	s_waitcnt lgkmcnt(0)
	v_fmac_f32_e32 v88, v92, v2
	v_fmac_f32_e32 v100, v92, v4
	v_mov_b32_e32 v92, v93
	v_mov_b32_e32 v93, v94
	ds_read_b32 v91, v64 offset:12480
	ds_read_b128 v[96:99], v77 offset:11456
	v_pk_mul_f32 v[94:95], v[92:93], v[18:19]
	v_pk_mul_f32 v[92:93], v[92:93], v[6:7]
	v_add_f32_e32 v84, v88, v94
	v_add_f32_e32 v88, v84, v95
	v_add_f32_e32 v84, v100, v92
	v_add_f32_e32 v84, v84, v93
	ds_read_b32 v106, v64 offset:12544
	ds_read_b128 v[92:95], v77 offset:11520
	ds_read_b64 v[100:101], v77 offset:11536
	s_waitcnt lgkmcnt(3)
	v_pk_mul_f32 v[102:103], v[96:97], v[2:3]
	v_pk_mul_f32 v[96:97], v[96:97], v[4:5]
	v_fma_f32 v85, v86, v85, v102
	v_add_f32_e32 v86, v91, v96
	v_add_f32_e32 v85, v85, v103
	v_add_f32_e32 v86, v86, v97
	v_pk_mul_f32 v[96:97], v[98:99], v[20:21]
	s_waitcnt lgkmcnt(1)
	v_fmac_f32_e32 v87, v92, v2
	v_add_f32_e32 v85, v85, v96
	v_add_f32_e32 v91, v85, v97
	v_pk_mul_f32 v[96:97], v[98:99], v[10:11]
	v_fmac_f32_e32 v106, v92, v4
	v_mov_b32_e32 v92, v93
	v_mov_b32_e32 v93, v94
	v_add_f32_e32 v85, v86, v96
	v_pk_mul_f32 v[102:103], v[92:93], v[18:19]
	v_add_f32_e32 v85, v85, v97
	v_add_f32_e32 v86, v87, v102
	v_add_f32_e32 v94, v86, v103
	v_pk_mul_f32 v[86:87], v[92:93], v[6:7]
	ds_read_b32 v108, v64 offset:12608
	ds_read_b128 v[96:99], v77 offset:11584
	ds_read_b64 v[104:105], v77 offset:11600
	v_add_f32_e32 v86, v106, v86
	v_mov_b32_e32 v92, v95
	s_waitcnt lgkmcnt(3)
	v_mov_b32_e32 v93, v100
	v_add_f32_e32 v101, v86, v87
	v_pk_mul_f32 v[86:87], v[92:93], v[24:25]
	v_pk_mul_f32 v[92:93], v[92:93], v[12:13]
	v_add_f32_e32 v86, v94, v86
	v_add_f32_e32 v87, v86, v87
	v_add_f32_e32 v86, v101, v92
	v_add_f32_e32 v86, v86, v93
	s_waitcnt lgkmcnt(1)
	v_pk_mul_f32 v[106:107], v[96:97], v[2:3]
	v_pk_mul_f32 v[96:97], v[96:97], v[4:5]
	v_fma_f32 v81, v82, v81, v106
	v_add_f32_e32 v82, v108, v96
	ds_read_b32 v110, v64 offset:12672
	ds_read_b128 v[92:95], v77 offset:11648
	ds_read_b128 v[100:103], v77 offset:11664
	v_add_f32_e32 v81, v81, v107
	v_add_f32_e32 v82, v82, v97
	v_pk_mul_f32 v[96:97], v[98:99], v[20:21]
	s_waitcnt lgkmcnt(1)
	v_fmac_f32_e32 v80, v92, v2
	v_add_f32_e32 v81, v81, v96
	v_add_f32_e32 v81, v81, v97
	v_pk_mul_f32 v[96:97], v[98:99], v[10:11]
	v_fmac_f32_e32 v110, v92, v4
	v_add_f32_e32 v82, v82, v96
	v_add_f32_e32 v98, v82, v97
	v_pk_mul_f32 v[96:97], v[104:105], v[28:29]
	v_mov_b32_e32 v92, v93
	v_mov_b32_e32 v93, v94
	v_add_f32_e32 v81, v81, v96
	v_pk_mul_f32 v[108:109], v[92:93], v[18:19]
	v_pk_mul_f32 v[92:93], v[92:93], v[6:7]
	v_add_f32_e32 v82, v81, v97
	v_pk_mul_f32 v[96:97], v[104:105], v[14:15]
	v_add_f32_e32 v92, v110, v92
	v_add_f32_e32 v81, v98, v96
	v_add_f32_e32 v80, v80, v108
	s_waitcnt lgkmcnt(0)
	v_add_f32_e32 v103, v92, v93
	v_mov_b32_e32 v92, v95
	v_mov_b32_e32 v93, v100
	v_add_f32_e32 v81, v81, v97
	v_add_f32_e32 v80, v80, v109
	v_pk_mul_f32 v[94:95], v[92:93], v[24:25]
	v_pk_mul_f32 v[92:93], v[92:93], v[12:13]
	v_add_f32_e32 v80, v80, v94
	ds_read_b32 v114, v64 offset:12736
	ds_read_b128 v[96:99], v77 offset:11712
	ds_read_b128 v[104:107], v77 offset:11728
	v_add_f32_e32 v80, v80, v95
	v_add_f32_e32 v92, v103, v92
	v_mov_b32_e32 v94, v101
	v_mov_b32_e32 v95, v102
	v_add_f32_e32 v100, v92, v93
	v_pk_mul_f32 v[92:93], v[94:95], v[30:31]
	v_pk_mul_f32 v[94:95], v[94:95], v[16:17]
	v_add_f32_e32 v80, v80, v92
	v_add_f32_e32 v92, v80, v93
	v_add_f32_e32 v80, v100, v94
	v_add_f32_e32 v80, v80, v95
	s_waitcnt lgkmcnt(1)
	v_pk_mul_f32 v[94:95], v[96:97], v[2:3]
	ds_read_b32 v93, v64 offset:12800
	ds_read_b128 v[100:103], v77 offset:11776
	ds_read_b128 v[108:111], v77 offset:11792
	ds_read_b64 v[112:113], v77 offset:11808
	v_fma_f32 v78, v79, v78, v94
	v_add_f32_e32 v94, v78, v95
	v_pk_mul_f32 v[78:79], v[96:97], v[4:5]
	s_waitcnt lgkmcnt(2)
; #define LAS __attribute__((address_space(3)))
; __global__ void __launch_bounds__(NWAVES * 64, 2) mk_fwd(Args args) {
;     ...
;                     rc = NB_[768 + c16]; nc[0] = *(const LAS f32x4*)(NB_ + 512);
; #pragma unroll
;                     for (int t = 0; t < 16; ++t) {
;                         if (t < 15) { rn = NB_[768 + (t + 1) * 16 + c16];
; #pragma unroll
;                             for (int sq = 0; sq < (t + 5) / 4; ++sq) nn[sq] = *(const LAS f32x4*)(NB_ + 512 + (t + 1) * 16 + 4 * sq); }
;                         float x3 = rt[t], x4 = rc;
; #pragma unroll
;                         for (int sq = 0; sq < (t + 4) / 4; ++sq) {
; #pragma unroll
;                             for (int e = 0; e < 4; ++e) if (4 * sq + e <= t) { x3 += nc[sq][e] * at[4 * sq + e]; x4 += nc[sq][e] * a2[4 * sq + e]; } }
;                         asm volatile("" : "+v"(x3), "+v"(x4) :: "memory");
;                         rt[t] = x3; a4[t] = x4; rc = rn;
; #pragma unroll
;                         for (int q = 0; q < 4; ++q) nc[q] = nn[q];
;                     }
	v_fmac_f32_e32 v76, v100, v2
	v_add_f32_e32 v78, v114, v78
	v_add_f32_e32 v95, v78, v79
	v_pk_mul_f32 v[78:79], v[98:99], v[20:21]
	v_fmac_f32_e32 v93, v100, v4
	v_add_f32_e32 v78, v94, v78
	v_add_f32_e32 v94, v78, v79
	v_pk_mul_f32 v[78:79], v[98:99], v[10:11]
	v_mov_b32_e32 v98, v101
	v_add_f32_e32 v78, v95, v78
	v_add_f32_e32 v95, v78, v79
	v_pk_mul_f32 v[78:79], v[104:105], v[28:29]
	v_mov_b32_e32 v99, v102
	v_add_f32_e32 v78, v94, v78
	v_add_f32_e32 v94, v78, v79
	v_pk_mul_f32 v[78:79], v[104:105], v[14:15]
	v_pk_mul_f32 v[100:101], v[98:99], v[18:19]
	v_add_f32_e32 v78, v95, v78
	v_add_f32_e32 v96, v78, v79
	v_pk_mul_f32 v[78:79], v[106:107], v[34:35]
	v_pk_mul_f32 v[98:99], v[98:99], v[6:7]
	v_add_f32_e32 v78, v94, v78
	v_pk_mul_f32 v[94:95], v[106:107], v[22:23]
	v_add_f32_e32 v79, v78, v79
	v_add_f32_e32 v78, v96, v94
	v_add_f32_e32 v78, v78, v95
	ds_read_b32 v118, v64 offset:12864
	ds_read_b128 v[94:97], v77 offset:11840
	ds_read_b128 v[104:107], v77 offset:11856
	ds_read_b64 v[116:117], v77 offset:11872
	v_add_f32_e32 v6, v93, v98
	v_add_f32_e32 v18, v76, v100
	s_waitcnt lgkmcnt(2)
	v_fmac_f32_e32 v75, v94, v2
	v_fmac_f32_e32 v118, v94, v4
	v_fmac_f32_e32 v75, v95, v3
	v_fmac_f32_e32 v118, v95, v5
	v_pk_mul_f32 v[94:95], v[96:97], v[20:21]
	v_add_f32_e32 v6, v6, v99
	v_add_f32_e32 v20, v75, v94
	v_mov_b32_e32 v98, v103
	v_mov_b32_e32 v99, v108
	v_add_f32_e32 v20, v20, v95
	v_pk_mul_f32 v[94:95], v[96:97], v[10:11]
	v_add_f32_e32 v18, v18, v101
	v_pk_mul_f32 v[100:101], v[98:99], v[24:25]
	v_pk_mul_f32 v[98:99], v[98:99], v[12:13]
	v_add_f32_e32 v10, v118, v94
	v_add_f32_e32 v6, v6, v98
	v_add_f32_e32 v10, v10, v95
	s_waitcnt lgkmcnt(1)
	v_pk_mul_f32 v[94:95], v[104:105], v[28:29]
	v_add_f32_e32 v18, v18, v100
	v_add_f32_e32 v6, v6, v99
	v_mov_b32_e32 v98, v109
	v_mov_b32_e32 v99, v110
	v_add_f32_e32 v20, v20, v94
	v_add_f32_e32 v18, v18, v101
	v_pk_mul_f32 v[100:101], v[98:99], v[30:31]
	v_pk_mul_f32 v[98:99], v[98:99], v[16:17]
	v_add_f32_e32 v20, v20, v95
	v_pk_mul_f32 v[94:95], v[104:105], v[14:15]
	v_add_f32_e32 v6, v6, v98
	v_add_f32_e32 v10, v10, v94
	v_add_f32_e32 v18, v18, v100
	v_add_f32_e32 v6, v6, v99
	v_mov_b32_e32 v98, v111
	v_mov_b32_e32 v99, v112
	v_add_f32_e32 v10, v10, v95
	v_pk_mul_f32 v[94:95], v[106:107], v[34:35]
	v_add_f32_e32 v18, v18, v101
	v_pk_mul_f32 v[100:101], v[98:99], v[38:39]
	v_pk_mul_f32 v[98:99], v[98:99], v[26:27]
	v_add_f32_e32 v20, v20, v94
	v_add_f32_e32 v18, v18, v100
	v_add_f32_e32 v6, v6, v98
	v_add_f32_e32 v20, v20, v95
	v_pk_mul_f32 v[94:95], v[106:107], v[22:23]
	v_add_f32_e32 v76, v18, v101
	v_add_f32_e32 v6, v6, v99
	v_add_f32_e32 v10, v10, v94
	v_add_f32_e32 v10, v10, v95
	s_waitcnt lgkmcnt(0)
	v_pk_mul_f32 v[94:95], v[116:117], v[42:43]
	ds_read_b32 v18, v64 offset:12928
	ds_read_b128 v[98:101], v77 offset:11904
	ds_read_b128 v[108:111], v77 offset:11920
	ds_read_b128 v[112:115], v77 offset:11936
	v_add_f32_e32 v20, v20, v94
	v_add_f32_e32 v93, v20, v95
	v_pk_mul_f32 v[94:95], v[116:117], v[32:33]
	s_waitcnt lgkmcnt(2)
	v_fmac_f32_e32 v74, v98, v2
	v_add_f32_e32 v10, v10, v94
	v_add_f32_e32 v10, v10, v95
	v_fmac_f32_e32 v18, v98, v4
	v_fmac_f32_e32 v74, v99, v3
	v_fmac_f32_e32 v18, v99, v5
	v_mov_b32_e32 v98, v101
	s_waitcnt lgkmcnt(1)
	v_mov_b32_e32 v99, v108
	ds_read_b32 v20, v64 offset:12992
	ds_read_b128 v[94:97], v77 offset:11968
	ds_read_b128 v[102:105], v77 offset:11984
	ds_read_b128 v[116:119], v77 offset:12000
	v_fmac_f32_e32 v74, v100, v19
	v_fmac_f32_e32 v18, v100, v7
	v_pk_mul_f32 v[100:101], v[98:99], v[24:25]
	s_waitcnt lgkmcnt(2)
	v_fmac_f32_e32 v73, v94, v2
	v_add_f32_e32 v24, v74, v100
	v_pk_mul_f32 v[74:75], v[98:99], v[12:13]
	v_fmac_f32_e32 v73, v95, v3
	v_add_f32_e32 v12, v18, v74
	v_add_f32_e32 v12, v12, v75
	v_mov_b32_e32 v74, v109
	v_mov_b32_e32 v75, v110
	v_pk_mul_f32 v[98:99], v[74:75], v[30:31]
	v_pk_mul_f32 v[74:75], v[74:75], v[16:17]
	v_add_f32_e32 v24, v24, v101
	v_add_f32_e32 v12, v12, v74
	v_fmac_f32_e32 v20, v94, v4
	v_fmac_f32_e32 v73, v96, v19
	v_add_f32_e32 v18, v24, v98
	v_add_f32_e32 v12, v12, v75
	v_mov_b32_e32 v74, v111
	v_mov_b32_e32 v75, v112
	v_fmac_f32_e32 v20, v95, v5
	v_fmac_f32_e32 v73, v97, v21
	s_waitcnt lgkmcnt(1)
	v_pk_mul_f32 v[94:95], v[102:103], v[28:29]
	v_add_f32_e32 v18, v18, v99
	v_pk_mul_f32 v[98:99], v[74:75], v[38:39]
	v_pk_mul_f32 v[74:75], v[74:75], v[26:27]
	v_fmac_f32_e32 v20, v96, v7
	v_add_f32_e32 v28, v73, v94
	v_add_f32_e32 v12, v12, v74
	v_fmac_f32_e32 v20, v97, v11
	v_add_f32_e32 v28, v28, v95
	v_pk_mul_f32 v[94:95], v[102:103], v[14:15]
	v_add_f32_e32 v18, v18, v98
	v_add_f32_e32 v12, v12, v75
	v_mov_b32_e32 v74, v113
	v_mov_b32_e32 v75, v114
	v_add_f32_e32 v14, v20, v94
	v_add_f32_e32 v18, v18, v99
	v_pk_mul_f32 v[98:99], v[74:75], v[44:45]
	v_pk_mul_f32 v[74:75], v[74:75], v[36:37]
	v_add_f32_e32 v14, v14, v95
	v_pk_mul_f32 v[94:95], v[104:105], v[34:35]
	v_add_f32_e32 v18, v18, v98
	v_add_f32_e32 v12, v12, v74
	v_add_f32_e32 v20, v28, v94
	v_add_f32_e32 v24, v18, v99
	v_add_f32_e32 v12, v12, v75
	v_add_f32_e32 v20, v20, v95
	v_pk_mul_f32 v[94:95], v[104:105], v[22:23]
	ds_read_b32 v18, v64 offset:13056
	ds_read_b128 v[98:101], v77 offset:12032
	ds_read_b128 v[106:109], v77 offset:12048
	ds_read_b128 v[110:113], v77 offset:12064
	ds_read_b64 v[74:75], v77 offset:12080
	v_add_f32_e32 v14, v14, v94
	v_add_f32_e32 v14, v14, v95
	s_waitcnt lgkmcnt(5)
	v_pk_mul_f32 v[94:95], v[116:117], v[42:43]
	s_waitcnt lgkmcnt(3)
; #define LAS __attribute__((address_space(3)))
; __global__ void __launch_bounds__(NWAVES * 64, 2) mk_fwd(Args args) {
;     ...
;                     rc = NB_[768 + c16]; nc[0] = *(const LAS f32x4*)(NB_ + 512);
; #pragma unroll
;                     for (int t = 0; t < 16; ++t) {
;                         if (t < 15) { rn = NB_[768 + (t + 1) * 16 + c16];
; #pragma unroll
;                             for (int sq = 0; sq < (t + 5) / 4; ++sq) nn[sq] = *(const LAS f32x4*)(NB_ + 512 + (t + 1) * 16 + 4 * sq); }
;                         float x3 = rt[t], x4 = rc;
; #pragma unroll
;                         for (int sq = 0; sq < (t + 4) / 4; ++sq) {
; #pragma unroll
;                             for (int e = 0; e < 4; ++e) if (4 * sq + e <= t) { x3 += nc[sq][e] * at[4 * sq + e]; x4 += nc[sq][e] * a2[4 * sq + e]; } }
;                         asm volatile("" : "+v"(x3), "+v"(x4) :: "memory");
;                         rt[t] = x3; a4[t] = x4; rc = rn;
; #pragma unroll
;                         for (int q = 0; q < 4; ++q) nc[q] = nn[q];
;                     }
	v_fmac_f32_e32 v72, v98, v2
	v_add_f32_e32 v20, v20, v94
	v_add_f32_e32 v20, v20, v95
	v_pk_mul_f32 v[94:95], v[116:117], v[32:33]
	v_fmac_f32_e32 v18, v98, v4
	v_add_f32_e32 v14, v14, v94
	v_fmac_f32_e32 v72, v99, v3
	v_add_f32_e32 v14, v14, v95
	v_pk_mul_f32 v[94:95], v[118:119], v[48:49]
	v_fmac_f32_e32 v18, v99, v5
	v_fmac_f32_e32 v72, v100, v19
	v_add_f32_e32 v20, v20, v94
	v_fmac_f32_e32 v18, v100, v7
	v_fmac_f32_e32 v72, v101, v21
	s_waitcnt lgkmcnt(2)
	v_mov_b32_e32 v98, v107
	v_mov_b32_e32 v99, v108
	v_add_f32_e32 v28, v20, v95
	v_pk_mul_f32 v[94:95], v[118:119], v[40:41]
	v_fmac_f32_e32 v18, v101, v11
	v_fmac_f32_e32 v72, v106, v25
	v_pk_mul_f32 v[100:101], v[98:99], v[30:31]
	v_add_f32_e32 v14, v14, v94
	v_fmac_f32_e32 v18, v106, v13
	v_add_f32_e32 v30, v72, v100
	v_pk_mul_f32 v[72:73], v[98:99], v[16:17]
	v_add_f32_e32 v14, v14, v95
	v_add_f32_e32 v16, v18, v72
	v_add_f32_e32 v16, v16, v73
	v_mov_b32_e32 v72, v109
	s_waitcnt lgkmcnt(1)
	v_mov_b32_e32 v73, v110
	ds_read_b32 v20, v64 offset:13120
	ds_read_b128 v[94:97], v77 offset:12096
	ds_read_b128 v[102:105], v77 offset:12112
	ds_read_b128 v[114:117], v77 offset:12128
	ds_read_b64 v[118:119], v77 offset:12144
	v_pk_mul_f32 v[98:99], v[72:73], v[38:39]
	v_pk_mul_f32 v[72:73], v[72:73], v[26:27]
	v_add_f32_e32 v30, v30, v101
	v_add_f32_e32 v16, v16, v72
	v_add_f32_e32 v18, v30, v98
	v_add_f32_e32 v16, v16, v73
	v_mov_b32_e32 v72, v111
	v_mov_b32_e32 v73, v112
	s_waitcnt lgkmcnt(3)
	v_fmac_f32_e32 v71, v94, v2
	v_add_f32_e32 v18, v18, v99
	v_pk_mul_f32 v[98:99], v[72:73], v[44:45]
	v_pk_mul_f32 v[72:73], v[72:73], v[36:37]
	v_fmac_f32_e32 v71, v95, v3
	v_add_f32_e32 v16, v16, v72
	v_fmac_f32_e32 v20, v94, v4
	v_fmac_f32_e32 v71, v96, v19
	v_add_f32_e32 v18, v18, v98
	v_add_f32_e32 v16, v16, v73
	v_mov_b32_e32 v72, v113
	v_mov_b32_e32 v73, v74
	v_fmac_f32_e32 v20, v95, v5
	v_fmac_f32_e32 v71, v97, v21
	v_add_f32_e32 v18, v18, v99
	v_pk_mul_f32 v[74:75], v[72:73], v[52:53]
	v_fmac_f32_e32 v20, v96, v7
	s_waitcnt lgkmcnt(2)
	v_fmac_f32_e32 v71, v102, v25
	v_add_f32_e32 v18, v18, v74
	v_fmac_f32_e32 v20, v97, v11
	v_fmac_f32_e32 v71, v103, v29
	v_pk_mul_f32 v[94:95], v[104:105], v[34:35]
	v_add_f32_e32 v30, v18, v75
	v_fmac_f32_e32 v20, v102, v13
	v_add_f32_e32 v18, v71, v94
	v_fmac_f32_e32 v20, v103, v15
	v_add_f32_e32 v18, v18, v95
	v_pk_mul_f32 v[94:95], v[104:105], v[22:23]
	v_pk_mul_f32 v[72:73], v[72:73], v[46:47]
	v_add_f32_e32 v20, v20, v94
	v_add_f32_e32 v16, v16, v72
	v_add_f32_e32 v20, v20, v95
	s_waitcnt lgkmcnt(1)
	v_pk_mul_f32 v[94:95], v[114:115], v[42:43]
	v_add_f32_e32 v16, v16, v73
	v_add_f32_e32 v18, v18, v94
	v_add_f32_e32 v18, v18, v95
	v_pk_mul_f32 v[94:95], v[114:115], v[32:33]
	ds_read_b32 v122, v64 offset:13184
	ds_read_b128 v[72:75], v77 offset:12160
	ds_read_b128 v[98:101], v77 offset:12176
	ds_read_b128 v[106:109], v77 offset:12192
	ds_read_b128 v[110:113], v77 offset:12208
	v_add_f32_e32 v20, v20, v94
	v_add_f32_e32 v20, v20, v95
	v_pk_mul_f32 v[94:95], v[116:117], v[48:49]
	s_waitcnt lgkmcnt(3)
	v_fmac_f32_e32 v122, v72, v4
	v_add_f32_e32 v18, v18, v94
	v_add_f32_e32 v18, v18, v95
	v_pk_mul_f32 v[94:95], v[116:117], v[40:41]
	v_fmac_f32_e32 v62, v72, v2
	v_fmac_f32_e32 v122, v73, v5
	v_add_f32_e32 v20, v20, v94
	v_fmac_f32_e32 v62, v73, v3
	v_fmac_f32_e32 v122, v74, v7
	v_add_f32_e32 v20, v20, v95
	v_pk_mul_f32 v[94:95], v[118:119], v[56:57]
	v_fmac_f32_e32 v62, v74, v19
	v_fmac_f32_e32 v122, v75, v11
	v_add_f32_e32 v18, v18, v94
	v_fmac_f32_e32 v62, v75, v21
	s_waitcnt lgkmcnt(2)
	v_fmac_f32_e32 v122, v98, v13
	v_add_f32_e32 v34, v18, v95
	v_pk_mul_f32 v[94:95], v[118:119], v[50:51]
	v_fmac_f32_e32 v62, v98, v25
	v_fmac_f32_e32 v122, v99, v15
	v_mov_b32_e32 v72, v101
	s_waitcnt lgkmcnt(1)
	v_mov_b32_e32 v73, v106
	v_add_f32_e32 v18, v20, v94
	v_fmac_f32_e32 v62, v99, v29
	v_fmac_f32_e32 v122, v100, v17
	v_pk_mul_f32 v[74:75], v[72:73], v[38:39]
	v_pk_mul_f32 v[72:73], v[72:73], v[26:27]
	v_add_f32_e32 v18, v18, v95
	v_fmac_f32_e32 v62, v100, v31
	v_add_f32_e32 v26, v122, v72
	v_add_f32_e32 v20, v62, v74
	v_add_f32_e32 v26, v26, v73
	v_mov_b32_e32 v72, v107
	v_mov_b32_e32 v73, v108
	ds_read_b32 v22, v64 offset:13248
	ds_read_b128 v[94:97], v77 offset:12224
	ds_read_b128 v[102:105], v77 offset:12240
	ds_read_b128 v[114:117], v77 offset:12256
	ds_read_b128 v[118:121], v77 offset:12272
	v_add_f32_e32 v20, v20, v75
	v_pk_mul_f32 v[74:75], v[72:73], v[44:45]
	v_pk_mul_f32 v[72:73], v[72:73], v[36:37]
	v_add_f32_e32 v20, v20, v74
	v_add_f32_e32 v26, v26, v72
	v_add_f32_e32 v26, v26, v73
	v_mov_b32_e32 v72, v109
	s_waitcnt lgkmcnt(5)
	v_mov_b32_e32 v73, v110
	s_waitcnt lgkmcnt(3)
	v_fmac_f32_e32 v58, v94, v2
	v_add_f32_e32 v20, v20, v75
	v_pk_mul_f32 v[74:75], v[72:73], v[52:53]
	v_pk_mul_f32 v[72:73], v[72:73], v[46:47]
	v_fmac_f32_e32 v58, v95, v3
	v_add_f32_e32 v26, v26, v72
	v_fmac_f32_e32 v22, v94, v4
	v_fmac_f32_e32 v58, v96, v19
	v_add_f32_e32 v20, v20, v74
	v_add_f32_e32 v26, v26, v73
	v_mov_b32_e32 v72, v111
	v_mov_b32_e32 v73, v112
	v_fmac_f32_e32 v22, v95, v5
	v_fmac_f32_e32 v58, v97, v21
	v_add_f32_e32 v20, v20, v75
	v_pk_mul_f32 v[74:75], v[72:73], v[60:61]
	v_fmac_f32_e32 v22, v96, v7
	s_waitcnt lgkmcnt(2)
	v_fmac_f32_e32 v58, v102, v25
	v_add_f32_e32 v20, v20, v74
	v_pk_mul_f32 v[72:73], v[72:73], v[54:55]
	v_fmac_f32_e32 v22, v97, v11
	v_fmac_f32_e32 v58, v103, v29
	v_add_f32_e32 v36, v20, v75
	v_add_f32_e32 v20, v26, v72
	v_fmac_f32_e32 v22, v102, v13
	v_fmac_f32_e32 v58, v104, v31
	v_add_f32_e32 v20, v20, v73
	v_fmac_f32_e32 v22, v103, v15
	v_fmac_f32_e32 v58, v105, v35
	s_waitcnt lgkmcnt(1)
; #define LAS __attribute__((address_space(3)))
; #define LDS_WAIT() asm volatile("s_waitcnt lgkmcnt(0)" ::: "memory")
; __device__ __forceinline__ unsigned cvt_nat(float lo, float hi) { const f32x2 v = {lo, hi}; return __builtin_bit_cast(unsigned, __builtin_convertvector(v, bf16n2)); }
; __global__ void __launch_bounds__(NWAVES * 64, 2) mk_fwd(Args args) {
;     ...
;                     rc = NB_[768 + c16]; nc[0] = *(const LAS f32x4*)(NB_ + 512);
; #pragma unroll
;                     for (int t = 0; t < 16; ++t) {
;                         if (t < 15) { rn = NB_[768 + (t + 1) * 16 + c16];
; #pragma unroll
;                             for (int sq = 0; sq < (t + 5) / 4; ++sq) nn[sq] = *(const LAS f32x4*)(NB_ + 512 + (t + 1) * 16 + 4 * sq); }
;                         float x3 = rt[t], x4 = rc;
; #pragma unroll
;                         for (int sq = 0; sq < (t + 4) / 4; ++sq) {
; #pragma unroll
;                             for (int e = 0; e < 4; ++e) if (4 * sq + e <= t) { x3 += nc[sq][e] * at[4 * sq + e]; x4 += nc[sq][e] * a2[4 * sq + e]; } }
;                         asm volatile("" : "+v"(x3), "+v"(x4) :: "memory");
;                         rt[t] = x3; a4[t] = x4; rc = rn;
; #pragma unroll
;                         for (int q = 0; q < 4; ++q) nc[q] = nn[q];
;                     }
;                 }
;                 LDS_WAIT(); asm volatile("" ::: "memory");
; #pragma unroll
;                 for (int t = 0; t < 16; ++t) { const int o = (((ln >> 3) ^ (t >> 1)) << 4) + (ln & 7) * 2;
;                     __builtin_amdgcn_raw_buffer_store_b16((bf16)(cvt_nat(at[t], 0.f) & 0xffffu), rs_o, o, t * 128, 0); __builtin_amdgcn_raw_buffer_store_b16((bf16)(cvt_nat(rt[t], 0.f) & 0xffffu), rs_o, o, 2048 + t * 128, 0); }
	v_pk_mul_f32 v[72:73], v[114:115], v[42:43]
	v_fmac_f32_e32 v22, v104, v17
	v_add_f32_e32 v26, v58, v72
	v_fmac_f32_e32 v22, v105, v23
	v_add_f32_e32 v26, v26, v73
	v_pk_mul_f32 v[72:73], v[114:115], v[32:33]
	v_mov_b32_e32 v62, v61
	v_add_f32_e32 v22, v22, v72
	v_add_f32_e32 v22, v22, v73
	v_pk_mul_f32 v[72:73], v[116:117], v[48:49]
	v_mov_b32_e32 v58, v55
	v_add_f32_e32 v26, v26, v72
	v_add_f32_e32 v26, v26, v73
	v_pk_mul_f32 v[72:73], v[116:117], v[40:41]
	v_cvt_pk_bf16_f32 v2, v2, s0
	v_add_f32_e32 v22, v22, v72
	v_add_f32_e32 v22, v22, v73
	s_waitcnt lgkmcnt(0)
	v_pk_mul_f32 v[72:73], v[118:119], v[56:57]
	s_nop 0
	v_add_f32_e32 v26, v26, v72
	v_add_f32_e32 v26, v26, v73
	v_pk_mul_f32 v[72:73], v[118:119], v[50:51]
	s_nop 0
	v_add_f32_e32 v22, v22, v72
	v_add_f32_e32 v22, v22, v73
	v_pk_mul_f32 v[72:73], v[120:121], v[62:63]
	s_nop 0
	v_add_f32_e32 v26, v26, v72
	v_add_f32_e32 v26, v26, v73
	v_pk_mul_f32 v[72:73], v[120:121], v[58:59]
	s_nop 0
	v_add_f32_e32 v22, v22, v72
	v_add_f32_e32 v22, v22, v73
	s_waitcnt lgkmcnt(0)
	buffer_store_short v2, v1, s[80:83], 0 offen
	v_cvt_pk_bf16_f32 v2, v70, s0
	buffer_store_short v2, v1, s[80:83], s16 offen
	v_cvt_pk_bf16_f32 v2, v3, s0
	buffer_store_short v2, v1, s[80:83], s73 offen
	v_cvt_pk_bf16_f32 v2, v90, s0
	s_movk_i32 s16, 0x880
	buffer_store_short v2, v1, s[80:83], s16 offen
	v_xor_b32_e32 v2, 16, v1
	v_cvt_pk_bf16_f32 v3, v19, s0
	s_movk_i32 s16, 0x100
	buffer_store_short v3, v2, s[80:83], s16 offen
	v_cvt_pk_bf16_f32 v3, v88, s0
	s_movk_i32 s16, 0x900
	buffer_store_short v3, v2, s[80:83], s16 offen
	v_cvt_pk_bf16_f32 v3, v21, s0
	s_movk_i32 s16, 0x180
	buffer_store_short v3, v2, s[80:83], s16 offen
	v_cvt_pk_bf16_f32 v3, v91, s0
	s_movk_i32 s16, 0x980
	buffer_store_short v3, v2, s[80:83], s16 offen
	v_xor_b32_e32 v2, 32, v1
	v_cvt_pk_bf16_f32 v3, v25, s0
	s_movk_i32 s16, 0x200
	buffer_store_short v3, v2, s[80:83], s16 offen
	v_cvt_pk_bf16_f32 v3, v87, s0
	s_movk_i32 s16, 0xa00
	buffer_store_short v3, v2, s[80:83], s16 offen
	v_cvt_pk_bf16_f32 v3, v29, s0
	s_movk_i32 s16, 0x280
	buffer_store_short v3, v2, s[80:83], s16 offen
	v_cvt_pk_bf16_f32 v3, v82, s0
	s_movk_i32 s16, 0xa80
	buffer_store_short v3, v2, s[80:83], s16 offen
	v_xor_b32_e32 v2, 48, v1
	v_cvt_pk_bf16_f32 v3, v31, s0
	buffer_store_short v3, v2, s[80:83], s74 offen
	v_cvt_pk_bf16_f32 v3, v92, s0
	s_movk_i32 s16, 0xb00
	buffer_store_short v3, v2, s[80:83], s16 offen
	v_cvt_pk_bf16_f32 v3, v35, s0
	s_movk_i32 s16, 0x380
	buffer_store_short v3, v2, s[80:83], s16 offen
	v_cvt_pk_bf16_f32 v3, v79, s0
	s_movk_i32 s16, 0xb80
	buffer_store_short v3, v2, s[80:83], s16 offen
	v_xor_b32_e32 v2, 64, v1
	v_cvt_pk_bf16_f32 v3, v39, s0
	s_movk_i32 s16, 0x400
	buffer_store_short v3, v2, s[80:83], s16 offen
	v_cvt_pk_bf16_f32 v3, v76, s0
	s_movk_i32 s16, 0xc00
	buffer_store_short v3, v2, s[80:83], s16 offen
	v_cvt_pk_bf16_f32 v3, v43, s0
	s_movk_i32 s16, 0x480
	buffer_store_short v3, v2, s[80:83], s16 offen
	v_cvt_pk_bf16_f32 v3, v93, s0
	s_movk_i32 s16, 0xc80
	buffer_store_short v3, v2, s[80:83], s16 offen
	v_xor_b32_e32 v2, 0x50, v1
	v_cvt_pk_bf16_f32 v3, v45, s0
	s_movk_i32 s16, 0x500
	buffer_store_short v3, v2, s[80:83], s16 offen
	v_cvt_pk_bf16_f32 v3, v24, s0
	s_movk_i32 s16, 0xd00
	buffer_store_short v3, v2, s[80:83], s16 offen
	v_cvt_pk_bf16_f32 v3, v49, s0
	s_movk_i32 s16, 0x580
	buffer_store_short v3, v2, s[80:83], s16 offen
	v_cvt_pk_bf16_f32 v3, v28, s0
	s_movk_i32 s16, 0xd80
	buffer_store_short v3, v2, s[80:83], s16 offen
	v_xor_b32_e32 v2, 0x60, v1
	v_cvt_pk_bf16_f32 v3, v53, s0
	s_movk_i32 s16, 0x600
	buffer_store_short v3, v2, s[80:83], s16 offen
	v_cvt_pk_bf16_f32 v3, v30, s0
	s_movk_i32 s16, 0xe00
	buffer_store_short v3, v2, s[80:83], s16 offen
	v_cvt_pk_bf16_f32 v3, v57, s0
	s_movk_i32 s16, 0x680
	buffer_store_short v3, v2, s[80:83], s16 offen
	v_cvt_pk_bf16_f32 v3, v34, s0
	s_movk_i32 s16, 0xe80
	buffer_store_short v3, v2, s[80:83], s16 offen
	v_xor_b32_e32 v2, 0x70, v1
	v_cvt_pk_bf16_f32 v3, v61, s0
	s_movk_i32 s16, 0x700
	buffer_store_short v3, v2, s[80:83], s16 offen
	v_cvt_pk_bf16_f32 v3, v36, s0
	s_movk_i32 s16, 0xf00
	buffer_store_short v3, v2, s[80:83], s16 offen
	v_cvt_pk_bf16_f32 v3, v63, s0
	s_movk_i32 s16, 0x780
	buffer_store_short v3, v2, s[80:83], s16 offen
	v_cvt_pk_bf16_f32 v3, v26, s0
	s_movk_i32 s16, 0xf80
	buffer_store_short v3, v2, s[80:83], s16 offen
	v_cmp_gt_i32_e64 s[16:17], 16, v0
	s_and_saveexec_b64 s[22:23], s[16:17]
	s_cbranch_execz .LBB0_748
; __device__ __forceinline__ unsigned cvt_nat(float lo, float hi) { const f32x2 v = {lo, hi}; return __builtin_bit_cast(unsigned, __builtin_convertvector(v, bf16n2)); }
; __global__ void __launch_bounds__(NWAVES * 64, 2) mk_fwd(Args args) {
;     ...
;                 if (ln < 16) {
; #pragma unroll
;                     for (int t = 0; t < 16; ++t) { const int o = (((ln >> 2) ^ (((t >> 3) & 1) << 1)) << 3) + (ln & 3) * 2;
;                         __builtin_amdgcn_raw_buffer_store_b16((bf16)(cvt_nat(a2[t], 0.f) & 0xffffu), rs_o, o, 10240 + t * 32, 0); __builtin_amdgcn_raw_buffer_store_b16((bf16)(cvt_nat(a4[t], 0.f) & 0xffffu), rs_o, o, 10752 + t * 32, 0); }
;                 }
	v_cvt_pk_bf16_f32 v0, v4, s0
	s_mov_b32 s80, s33
	s_movk_i32 s16, 0x2800
	buffer_store_short v0, v1, s[80:83], s16 offen
	v_cvt_pk_bf16_f32 v0, v89, s0
	s_movk_i32 s16, 0x2a00
	buffer_store_short v0, v1, s[80:83], s16 offen
	v_cvt_pk_bf16_f32 v0, v5, s0
	s_movk_i32 s16, 0x2820
	buffer_store_short v0, v1, s[80:83], s16 offen
	v_cvt_pk_bf16_f32 v0, v83, s0
	s_movk_i32 s16, 0x2a20
	buffer_store_short v0, v1, s[80:83], s16 offen
	v_cvt_pk_bf16_f32 v0, v7, s0
	s_movk_i32 s16, 0x2840
	buffer_store_short v0, v1, s[80:83], s16 offen
	v_cvt_pk_bf16_f32 v0, v84, s0
	s_movk_i32 s16, 0x2a40
	buffer_store_short v0, v1, s[80:83], s16 offen
	v_cvt_pk_bf16_f32 v0, v11, s0
	s_movk_i32 s16, 0x2860
	buffer_store_short v0, v1, s[80:83], s16 offen
	v_cvt_pk_bf16_f32 v0, v85, s0
	s_movk_i32 s16, 0x2a60
	buffer_store_short v0, v1, s[80:83], s16 offen
	v_cvt_pk_bf16_f32 v0, v13, s0
	s_movk_i32 s16, 0x2880
	buffer_store_short v0, v1, s[80:83], s16 offen
	v_cvt_pk_bf16_f32 v0, v86, s0
	s_movk_i32 s16, 0x2a80
	buffer_store_short v0, v1, s[80:83], s16 offen
	v_cvt_pk_bf16_f32 v0, v15, s0
	s_movk_i32 s16, 0x28a0
	buffer_store_short v0, v1, s[80:83], s16 offen
	v_cvt_pk_bf16_f32 v0, v81, s0
	s_movk_i32 s16, 0x2aa0
	buffer_store_short v0, v1, s[80:83], s16 offen
	v_cvt_pk_bf16_f32 v0, v17, s0
	s_movk_i32 s16, 0x28c0
	buffer_store_short v0, v1, s[80:83], s16 offen
	v_cvt_pk_bf16_f32 v0, v80, s0
	s_movk_i32 s16, 0x2ac0
	buffer_store_short v0, v1, s[80:83], s16 offen
	v_cvt_pk_bf16_f32 v0, v23, s0
	s_movk_i32 s16, 0x28e0
	buffer_store_short v0, v1, s[80:83], s16 offen
	v_cvt_pk_bf16_f32 v0, v78, s0
	s_movk_i32 s16, 0x2ae0
	buffer_store_short v0, v1, s[80:83], s16 offen
	v_bitop3_b32 v0, v1, 16, -2 bitop3:0x6c
	v_cvt_pk_bf16_f32 v1, v27, s0
	s_movk_i32 s16, 0x2900
	buffer_store_short v1, v0, s[80:83], s16 offen
	v_cvt_pk_bf16_f32 v1, v6, s0
	s_movk_i32 s16, 0x2b00
	buffer_store_short v1, v0, s[80:83], s16 offen
	v_cvt_pk_bf16_f32 v1, v33, s0
	s_movk_i32 s16, 0x2920
	buffer_store_short v1, v0, s[80:83], s16 offen
	v_cvt_pk_bf16_f32 v1, v10, s0
	s_movk_i32 s16, 0x2b20
	buffer_store_short v1, v0, s[80:83], s16 offen
	v_cvt_pk_bf16_f32 v1, v37, s0
	s_movk_i32 s16, 0x2940
	buffer_store_short v1, v0, s[80:83], s16 offen
	v_cvt_pk_bf16_f32 v1, v12, s0
	s_movk_i32 s16, 0x2b40
	buffer_store_short v1, v0, s[80:83], s16 offen
	v_cvt_pk_bf16_f32 v1, v41, s0
	s_movk_i32 s16, 0x2960
	buffer_store_short v1, v0, s[80:83], s16 offen
	v_cvt_pk_bf16_f32 v1, v14, s0
	s_movk_i32 s16, 0x2b60
	buffer_store_short v1, v0, s[80:83], s16 offen
	v_cvt_pk_bf16_f32 v1, v47, s0
	s_movk_i32 s16, 0x2980
	buffer_store_short v1, v0, s[80:83], s16 offen
	v_cvt_pk_bf16_f32 v1, v16, s0
	s_movk_i32 s16, 0x2b80
	buffer_store_short v1, v0, s[80:83], s16 offen
	v_cvt_pk_bf16_f32 v1, v51, s0
	s_movk_i32 s16, 0x29a0
	buffer_store_short v1, v0, s[80:83], s16 offen
	v_cvt_pk_bf16_f32 v1, v18, s0
	s_movk_i32 s16, 0x2ba0
	buffer_store_short v1, v0, s[80:83], s16 offen
	v_cvt_pk_bf16_f32 v1, v55, s0
	s_movk_i32 s16, 0x29c0
	buffer_store_short v1, v0, s[80:83], s16 offen
	v_cvt_pk_bf16_f32 v1, v20, s0
	s_movk_i32 s16, 0x2bc0
	buffer_store_short v1, v0, s[80:83], s16 offen
	v_cvt_pk_bf16_f32 v1, v59, s0
	s_movk_i32 s16, 0x29e0
	buffer_store_short v1, v0, s[80:83], s16 offen
	v_cvt_pk_bf16_f32 v1, v22, s0
	s_movk_i32 s16, 0x2be0
	buffer_store_short v1, v0, s[80:83], s16 offen
	s_branch .LBB0_748
